# GEMM tiles: first K-iteration peeled with C=0 on the first MFMA of each accumulator (no per-tile accumulator zeroing); plus indexer interleave and stick-breaking load hoist
# baseline (speedup 1.0000x reference)
.LBB0_400:
	s_ashr_i32 s15, s14, 31
	s_lshl_b64 s[16:17], s[14:15], 20
	s_add_u32 s16, s38, s16
	s_addc_u32 s17, s39, s17
	s_and_b64 s[18:19], s[8:9], exec
	s_cselect_b32 s15, s17, s21
	s_cselect_b32 s72, s16, s20
	s_ashr_i32 s13, s12, 31
	s_lshl_b64 s[18:19], s[12:13], 20
	s_add_u32 s18, s36, s18
	s_addc_u32 s19, s37, s19
	s_and_b64 s[34:35], s[8:9], exec
	s_cselect_b32 s13, s19, s31
	s_cselect_b32 s73, s18, s30
	s_add_u32 s20, s20, 0x80080
	s_addc_u32 s21, s21, 0
	s_add_u32 s76, s30, 0x100
	s_addc_u32 s77, s31, 0
	s_mov_b32 s84, -2
	s_add_u32 s30, s20, 0xfff80080
	s_addc_u32 s31, s21, -1
	s_add_i32 s65, 0, 0x10000
	s_cmp_eq_u32 s84, 28
	v_add_u32_e32 v149, s65, v140
	v_add_u32_e32 v154, s65, v144
	s_cselect_b32 s35, s15, s31
	s_cselect_b32 s34, s72, s30
	ds_read_b128 v[150:153], v149
	ds_read_b128 v[154:157], v154
	v_add_u32_e32 v149, s1, v140
	s_cselect_b32 s31, s13, s77
	s_cselect_b32 s30, s73, s76
	s_add_i32 s90, 0, 0x14000
	v_add_u32_e32 v158, s1, v144
	ds_read_b128 v[166:169], v149
	ds_read_b128 v[170:173], v158
	v_add_u32_e32 v149, s90, v140
	v_add_u32_e32 v158, s90, v144
	ds_read_b128 v[174:177], v149
	ds_read_b128 v[178:181], v158
	v_add_u32_e32 v149, s86, v140
	v_add_u32_e32 v158, s86, v144
	ds_read_b128 v[182:185], v149
	ds_read_b128 v[186:189], v158
	v_lshl_add_u64 v[158:159], s[20:21], 0, v[136:137]
	s_add_i32 m0, s43, 0xc000
	ds_read_b128 v[190:193], v145
	ds_read_b128 v[194:197], v145 offset:2048
	ds_read_b128 v[198:201], v146
	ds_read_b128 v[202:205], v146 offset:2048
	ds_read_b128 v[206:209], v145 offset:4096
	ds_read_b128 v[210:213], v145 offset:6144
	ds_read_b128 v[214:217], v146 offset:4096
	ds_read_b128 v[226:229], v146 offset:6144
	global_load_lds_dwordx4 v[158:159], off
	v_lshl_add_u64 v[158:159], s[20:21], 0, v[138:139]
	s_add_i32 m0, s43, 0xe000
	s_nop 0
	global_load_lds_dwordx4 v[158:159], off
	s_waitcnt vmcnt(8)
	s_waitcnt lgkmcnt(0)
	s_barrier
	s_setprio 1
	s_waitcnt lgkmcnt(0)
	v_mfma_f32_16x16x32_bf16 v[124:127], v[150:153], v[190:193], 0
	v_mfma_f32_16x16x32_bf16 v[120:123], v[166:169], v[190:193], 0
	v_mfma_f32_16x16x32_bf16 v[116:119], v[150:153], v[194:197], 0
	v_mfma_f32_16x16x32_bf16 v[112:115], v[166:169], v[194:197], 0
	v_mfma_f32_16x16x32_bf16 v[100:103], v[150:153], v[206:209], 0
	v_mfma_f32_16x16x32_bf16 v[96:99], v[166:169], v[206:209], 0
	v_mfma_f32_16x16x32_bf16 v[84:87], v[150:153], v[210:213], 0
	v_mfma_f32_16x16x32_bf16 v[76:79], v[166:169], v[210:213], 0
	v_mfma_f32_16x16x32_bf16 v[124:127], v[154:157], v[198:201], v[124:127]
	v_mfma_f32_16x16x32_bf16 v[120:123], v[170:173], v[198:201], v[120:123]
	v_mfma_f32_16x16x32_bf16 v[116:119], v[154:157], v[202:205], v[116:119]
	v_mfma_f32_16x16x32_bf16 v[112:115], v[170:173], v[202:205], v[112:115]
	v_mfma_f32_16x16x32_bf16 v[100:103], v[154:157], v[214:217], v[100:103]
	v_mfma_f32_16x16x32_bf16 v[96:99], v[170:173], v[214:217], v[96:99]
	v_mfma_f32_16x16x32_bf16 v[84:87], v[154:157], v[226:229], v[84:87]
	v_mfma_f32_16x16x32_bf16 v[76:79], v[170:173], v[226:229], v[76:79]
	s_setprio 0
	s_setprio 1
	v_mfma_f32_16x16x32_bf16 v[108:111], v[174:177], v[190:193], 0
	v_mfma_f32_16x16x32_bf16 v[104:107], v[182:185], v[190:193], 0
	v_mfma_f32_16x16x32_bf16 v[92:95], v[174:177], v[194:197], 0
	v_mfma_f32_16x16x32_bf16 v[88:91], v[182:185], v[194:197], 0
	v_mfma_f32_16x16x32_bf16 v[80:83], v[174:177], v[206:209], 0
	v_mfma_f32_16x16x32_bf16 v[72:75], v[182:185], v[206:209], 0
	v_mfma_f32_16x16x32_bf16 v[68:71], v[174:177], v[210:213], 0
	v_mfma_f32_16x16x32_bf16 v[64:67], v[182:185], v[210:213], 0
	v_mfma_f32_16x16x32_bf16 v[108:111], v[178:181], v[198:201], v[108:111]
	v_mfma_f32_16x16x32_bf16 v[104:107], v[186:189], v[198:201], v[104:107]
	v_mfma_f32_16x16x32_bf16 v[92:95], v[178:181], v[202:205], v[92:95]
	v_mfma_f32_16x16x32_bf16 v[88:91], v[186:189], v[202:205], v[88:91]
	v_mfma_f32_16x16x32_bf16 v[80:83], v[178:181], v[214:217], v[80:83]
	v_mfma_f32_16x16x32_bf16 v[72:75], v[186:189], v[214:217], v[72:75]
	v_mfma_f32_16x16x32_bf16 v[68:71], v[178:181], v[226:229], v[68:71]
	v_mfma_f32_16x16x32_bf16 v[64:67], v[186:189], v[226:229], v[64:67]
	s_setprio 0
	s_barrier
	s_add_i32 s65, s65, s41
	v_lshl_add_u64 v[158:159], s[30:31], 0, v[132:133]
	s_mov_b32 m0, s65
	ds_read_b128 v[190:193], v145 offset:16384
	ds_read_b128 v[194:197], v145 offset:18432
	ds_read_b128 v[198:201], v146 offset:16384
	ds_read_b128 v[202:205], v146 offset:18432
	ds_read_b128 v[206:209], v145 offset:20480
	ds_read_b128 v[210:213], v145 offset:22528
	ds_read_b128 v[214:217], v146 offset:20480
	ds_read_b128 v[226:229], v146 offset:22528
	global_load_lds_dwordx4 v[158:159], off
	s_add_i32 m0, s65, 0x2000
	s_add_u32 s88, s30, 0x20000
	v_lshl_add_u64 v[218:219], s[30:31], 0, v[128:129]
	s_addc_u32 s89, s31, 0
	s_add_i32 s65, s90, s41
	global_load_lds_dwordx4 v[218:219], off
	v_lshl_add_u64 v[230:231], s[88:89], 0, v[132:133]
	s_mov_b32 m0, s65
	v_lshl_add_u64 v[232:233], s[34:35], 0, v[130:131]
	global_load_lds_dwordx4 v[230:231], off
	v_lshl_add_u64 v[230:231], s[88:89], 0, v[128:129]
	s_add_i32 m0, s65, 0x2000
	s_nop 0
	global_load_lds_dwordx4 v[230:231], off
	v_lshl_add_u64 v[230:231], s[34:35], 0, v[134:135]
	s_mov_b32 m0, s43
	s_nop 0
	global_load_lds_dwordx4 v[230:231], off
	s_mov_b32 m0, s46
	s_nop 0
	global_load_lds_dwordx4 v[232:233], off
	s_waitcnt vmcnt(8)
	s_waitcnt lgkmcnt(0)
	s_barrier
	s_setprio 1
	s_waitcnt lgkmcnt(0)
	v_mfma_f32_16x16x32_bf16 v[60:63], v[150:153], v[190:193], 0
	v_mfma_f32_16x16x32_bf16 v[56:59], v[166:169], v[190:193], 0
	v_mfma_f32_16x16x32_bf16 v[52:55], v[150:153], v[194:197], 0
	v_mfma_f32_16x16x32_bf16 v[44:47], v[166:169], v[194:197], 0
	v_mfma_f32_16x16x32_bf16 v[36:39], v[150:153], v[206:209], 0
	v_mfma_f32_16x16x32_bf16 v[28:31], v[166:169], v[206:209], 0
	v_mfma_f32_16x16x32_bf16 v[20:23], v[150:153], v[210:213], 0
	v_mfma_f32_16x16x32_bf16 v[12:15], v[166:169], v[210:213], 0
	v_mfma_f32_16x16x32_bf16 v[60:63], v[154:157], v[198:201], v[60:63]
	v_mfma_f32_16x16x32_bf16 v[56:59], v[170:173], v[198:201], v[56:59]
	v_mfma_f32_16x16x32_bf16 v[52:55], v[154:157], v[202:205], v[52:55]
	v_mfma_f32_16x16x32_bf16 v[44:47], v[170:173], v[202:205], v[44:47]
	v_mfma_f32_16x16x32_bf16 v[36:39], v[154:157], v[214:217], v[36:39]
	v_mfma_f32_16x16x32_bf16 v[28:31], v[170:173], v[214:217], v[28:31]
	v_mfma_f32_16x16x32_bf16 v[20:23], v[154:157], v[226:229], v[20:23]
	v_mfma_f32_16x16x32_bf16 v[12:15], v[170:173], v[226:229], v[12:15]
	s_setprio 0
	s_setprio 1
	v_mfma_f32_16x16x32_bf16 v[48:51], v[174:177], v[190:193], 0
	v_mfma_f32_16x16x32_bf16 v[40:43], v[182:185], v[190:193], 0
	v_mfma_f32_16x16x32_bf16 v[32:35], v[174:177], v[194:197], 0
	v_mfma_f32_16x16x32_bf16 v[24:27], v[182:185], v[194:197], 0
	v_mfma_f32_16x16x32_bf16 v[16:19], v[174:177], v[206:209], 0
	v_mfma_f32_16x16x32_bf16 v[8:11], v[182:185], v[206:209], 0
	v_mfma_f32_16x16x32_bf16 v[4:7], v[174:177], v[210:213], 0
	v_mfma_f32_16x16x32_bf16 v[0:3], v[182:185], v[210:213], 0
	v_mfma_f32_16x16x32_bf16 v[48:51], v[178:181], v[198:201], v[48:51]
	v_mfma_f32_16x16x32_bf16 v[40:43], v[186:189], v[198:201], v[40:43]
	v_mfma_f32_16x16x32_bf16 v[32:35], v[178:181], v[202:205], v[32:35]
	v_mfma_f32_16x16x32_bf16 v[24:27], v[186:189], v[202:205], v[24:27]
	v_mfma_f32_16x16x32_bf16 v[16:19], v[178:181], v[214:217], v[16:19]
	v_mfma_f32_16x16x32_bf16 v[8:11], v[186:189], v[214:217], v[8:11]
	v_mfma_f32_16x16x32_bf16 v[4:7], v[178:181], v[226:229], v[4:7]
	v_mfma_f32_16x16x32_bf16 v[0:3], v[186:189], v[226:229], v[0:3]
	s_setprio 0
	s_barrier
	s_add_i32 s65, 0, 0x18000
	v_add_u32_e32 v149, s65, v140
	v_add_u32_e32 v154, s65, v144
	ds_read_b128 v[150:153], v149
	ds_read_b128 v[154:157], v154
	v_add_u32_e32 v149, s87, v140
	s_add_i32 s88, 0, 0x1c000
	v_add_u32_e32 v162, s87, v144
	ds_read_b128 v[166:169], v149
	ds_read_b128 v[170:173], v162
	v_add_u32_e32 v149, s88, v140
	v_add_u32_e32 v162, s88, v144
	ds_read_b128 v[174:177], v149
	ds_read_b128 v[178:181], v162
	v_add_u32_e32 v149, s2, v140
	v_add_u32_e32 v162, s2, v144
	ds_read_b128 v[182:185], v149
	ds_read_b128 v[186:189], v162
	s_add_u32 s34, s34, 0x80000
	s_addc_u32 s35, s35, 0
	s_mov_b32 m0, s47
	v_lshl_add_u64 v[234:235], s[34:35], 0, v[134:135]
	ds_read_b128 v[190:193], v145 offset:32768
	ds_read_b128 v[194:197], v145 offset:34816
	ds_read_b128 v[198:201], v146 offset:32768
	ds_read_b128 v[202:205], v146 offset:34816
	ds_read_b128 v[206:209], v145 offset:36864
	ds_read_b128 v[210:213], v145 offset:38912
	ds_read_b128 v[214:217], v146 offset:36864
	ds_read_b128 v[226:229], v146 offset:38912
	global_load_lds_dwordx4 v[234:235], off
	v_lshl_add_u64 v[234:235], s[34:35], 0, v[130:131]
	s_mov_b32 m0, s56
	s_nop 0
	global_load_lds_dwordx4 v[234:235], off
	s_waitcnt vmcnt(8)
	s_waitcnt lgkmcnt(0)
	s_barrier
	s_setprio 1
	s_waitcnt lgkmcnt(0)
	v_mfma_f32_16x16x32_bf16 v[124:127], v[150:153], v[190:193], v[124:127]
	v_mfma_f32_16x16x32_bf16 v[120:123], v[166:169], v[190:193], v[120:123]
	v_mfma_f32_16x16x32_bf16 v[116:119], v[150:153], v[194:197], v[116:119]
	v_mfma_f32_16x16x32_bf16 v[112:115], v[166:169], v[194:197], v[112:115]
	v_mfma_f32_16x16x32_bf16 v[100:103], v[150:153], v[206:209], v[100:103]
	v_mfma_f32_16x16x32_bf16 v[96:99], v[166:169], v[206:209], v[96:99]
	v_mfma_f32_16x16x32_bf16 v[84:87], v[150:153], v[210:213], v[84:87]
	v_mfma_f32_16x16x32_bf16 v[76:79], v[166:169], v[210:213], v[76:79]
	v_mfma_f32_16x16x32_bf16 v[124:127], v[154:157], v[198:201], v[124:127]
	v_mfma_f32_16x16x32_bf16 v[120:123], v[170:173], v[198:201], v[120:123]
	v_mfma_f32_16x16x32_bf16 v[116:119], v[154:157], v[202:205], v[116:119]
	v_mfma_f32_16x16x32_bf16 v[112:115], v[170:173], v[202:205], v[112:115]
	v_mfma_f32_16x16x32_bf16 v[100:103], v[154:157], v[214:217], v[100:103]
	v_mfma_f32_16x16x32_bf16 v[96:99], v[170:173], v[214:217], v[96:99]
	v_mfma_f32_16x16x32_bf16 v[84:87], v[154:157], v[226:229], v[84:87]
	v_mfma_f32_16x16x32_bf16 v[76:79], v[170:173], v[226:229], v[76:79]
	s_setprio 0
	s_setprio 1
	v_mfma_f32_16x16x32_bf16 v[108:111], v[174:177], v[190:193], v[108:111]
	v_mfma_f32_16x16x32_bf16 v[104:107], v[182:185], v[190:193], v[104:107]
	v_mfma_f32_16x16x32_bf16 v[92:95], v[174:177], v[194:197], v[92:95]
	v_mfma_f32_16x16x32_bf16 v[88:91], v[182:185], v[194:197], v[88:91]
	v_mfma_f32_16x16x32_bf16 v[80:83], v[174:177], v[206:209], v[80:83]
	v_mfma_f32_16x16x32_bf16 v[72:75], v[182:185], v[206:209], v[72:75]
	v_mfma_f32_16x16x32_bf16 v[68:71], v[174:177], v[210:213], v[68:71]
	v_mfma_f32_16x16x32_bf16 v[64:67], v[182:185], v[210:213], v[64:67]
	v_mfma_f32_16x16x32_bf16 v[108:111], v[178:181], v[198:201], v[108:111]
	v_mfma_f32_16x16x32_bf16 v[104:107], v[186:189], v[198:201], v[104:107]
	v_mfma_f32_16x16x32_bf16 v[92:95], v[178:181], v[202:205], v[92:95]
	v_mfma_f32_16x16x32_bf16 v[88:91], v[186:189], v[202:205], v[88:91]
	v_mfma_f32_16x16x32_bf16 v[80:83], v[178:181], v[214:217], v[80:83]
	v_mfma_f32_16x16x32_bf16 v[72:75], v[186:189], v[214:217], v[72:75]
	v_mfma_f32_16x16x32_bf16 v[68:71], v[178:181], v[226:229], v[68:71]
	v_mfma_f32_16x16x32_bf16 v[64:67], v[186:189], v[226:229], v[64:67]
	s_setprio 0
	s_barrier
	s_add_i32 s34, s65, s41
	v_lshl_add_u64 v[158:159], v[158:159], 0, s[54:55]
	s_mov_b32 m0, s34
	ds_read_b128 v[190:193], v145 offset:49152
	ds_read_b128 v[194:197], v145 offset:51200
	ds_read_b128 v[198:201], v146 offset:49152
	ds_read_b128 v[202:205], v146 offset:51200
	ds_read_b128 v[206:209], v145 offset:53248
	ds_read_b128 v[210:213], v145 offset:55296
	ds_read_b128 v[214:217], v146 offset:53248
	ds_read_b128 v[226:229], v146 offset:55296
	global_load_lds_dwordx4 v[158:159], off
	s_add_i32 m0, s34, 0x2000
	s_add_u32 s30, s30, 0x20080
	v_lshl_add_u64 v[158:159], v[218:219], 0, s[54:55]
	s_addc_u32 s31, s31, 0
	s_add_i32 s34, s88, s41
	global_load_lds_dwordx4 v[158:159], off
	v_lshl_add_u64 v[158:159], s[30:31], 0, v[132:133]
	s_mov_b32 m0, s34
	s_nop 0
	global_load_lds_dwordx4 v[158:159], off
	v_lshl_add_u64 v[158:159], s[30:31], 0, v[128:129]
	s_add_i32 m0, s34, 0x2000
	s_nop 0
	global_load_lds_dwordx4 v[158:159], off
	v_lshl_add_u64 v[158:159], v[230:231], 0, s[54:55]
	s_mov_b32 m0, s57
	s_nop 0
	global_load_lds_dwordx4 v[158:159], off
	v_lshl_add_u64 v[158:159], v[232:233], 0, s[54:55]
	s_mov_b32 m0, s58
	s_nop 0
	global_load_lds_dwordx4 v[158:159], off
	s_waitcnt vmcnt(8)
	s_waitcnt lgkmcnt(0)
	s_barrier
	s_setprio 1
	s_waitcnt lgkmcnt(0)
	v_mfma_f32_16x16x32_bf16 v[60:63], v[150:153], v[190:193], v[60:63]
	v_mfma_f32_16x16x32_bf16 v[56:59], v[166:169], v[190:193], v[56:59]
	v_mfma_f32_16x16x32_bf16 v[52:55], v[150:153], v[194:197], v[52:55]
	v_mfma_f32_16x16x32_bf16 v[44:47], v[166:169], v[194:197], v[44:47]
	v_mfma_f32_16x16x32_bf16 v[36:39], v[150:153], v[206:209], v[36:39]
	v_mfma_f32_16x16x32_bf16 v[28:31], v[166:169], v[206:209], v[28:31]
	v_mfma_f32_16x16x32_bf16 v[20:23], v[150:153], v[210:213], v[20:23]
	v_mfma_f32_16x16x32_bf16 v[12:15], v[166:169], v[210:213], v[12:15]
	v_mfma_f32_16x16x32_bf16 v[60:63], v[154:157], v[198:201], v[60:63]
	v_mfma_f32_16x16x32_bf16 v[56:59], v[170:173], v[198:201], v[56:59]
	v_mfma_f32_16x16x32_bf16 v[52:55], v[154:157], v[202:205], v[52:55]
	v_mfma_f32_16x16x32_bf16 v[44:47], v[170:173], v[202:205], v[44:47]
	v_mfma_f32_16x16x32_bf16 v[36:39], v[154:157], v[214:217], v[36:39]
	v_mfma_f32_16x16x32_bf16 v[28:31], v[170:173], v[214:217], v[28:31]
	v_mfma_f32_16x16x32_bf16 v[20:23], v[154:157], v[226:229], v[20:23]
	v_mfma_f32_16x16x32_bf16 v[12:15], v[170:173], v[226:229], v[12:15]
	s_setprio 0
	s_setprio 1
	v_mfma_f32_16x16x32_bf16 v[48:51], v[174:177], v[190:193], v[48:51]
	v_mfma_f32_16x16x32_bf16 v[40:43], v[182:185], v[190:193], v[40:43]
	v_mfma_f32_16x16x32_bf16 v[32:35], v[174:177], v[194:197], v[32:35]
	v_mfma_f32_16x16x32_bf16 v[24:27], v[182:185], v[194:197], v[24:27]
	v_mfma_f32_16x16x32_bf16 v[16:19], v[174:177], v[206:209], v[16:19]
	v_mfma_f32_16x16x32_bf16 v[8:11], v[182:185], v[206:209], v[8:11]
	v_mfma_f32_16x16x32_bf16 v[4:7], v[174:177], v[210:213], v[4:7]
	v_mfma_f32_16x16x32_bf16 v[0:3], v[182:185], v[210:213], v[0:3]
	v_mfma_f32_16x16x32_bf16 v[48:51], v[178:181], v[198:201], v[48:51]
	v_mfma_f32_16x16x32_bf16 v[40:43], v[186:189], v[198:201], v[40:43]
	v_mfma_f32_16x16x32_bf16 v[32:35], v[178:181], v[202:205], v[32:35]
	v_mfma_f32_16x16x32_bf16 v[24:27], v[186:189], v[202:205], v[24:27]
	v_mfma_f32_16x16x32_bf16 v[16:19], v[178:181], v[214:217], v[16:19]
	v_mfma_f32_16x16x32_bf16 v[8:11], v[186:189], v[214:217], v[8:11]
	v_mfma_f32_16x16x32_bf16 v[4:7], v[178:181], v[226:229], v[4:7]
	v_mfma_f32_16x16x32_bf16 v[0:3], v[186:189], v[226:229], v[0:3]
	s_setprio 0
	s_barrier
	s_add_i32 s84, s84, 2
	s_add_u32 s20, s20, 0x100
	s_addc_u32 s21, s21, 0
	s_add_u32 s76, s76, 0x100
	s_addc_u32 s77, s77, 0
	s_cmp_gt_u32 s84, 29
	s_cbranch_scc1 .Lepi_401

.Lepi_401:
	s_and_b64 vcc, exec, s[10:11]
	s_cbranch_vccz .LBB0_404
	s_barrier

.LBB0_500:
	s_ashr_i32 s17, s16, 31
	s_lshl_b64 s[18:19], s[16:17], 20
	s_add_u32 s18, s52, s18
	s_addc_u32 s19, s53, s19
	s_and_b64 s[20:21], s[8:9], exec
	s_cselect_b32 s17, s19, s31
	s_cselect_b32 s76, s18, s30
	s_ashr_i32 s15, s14, 31
	s_lshl_b64 s[20:21], s[14:15], 20
	s_add_u32 s20, s41, s20
	s_addc_u32 s21, s43, s21
	s_and_b64 s[36:37], s[8:9], exec
	s_cselect_b32 s15, s21, s35
	s_cselect_b32 s77, s20, s34
	s_add_u32 s30, s30, 0x80080
	s_addc_u32 s31, s31, 0
	s_add_u32 s84, s34, 0x100
	s_addc_u32 s88, s35, 0
	s_mov_b32 s89, -2
	s_add_u32 s34, s30, 0xfff80080
	s_addc_u32 s35, s31, -1
	s_add_i32 s65, 0, 0x10000
	s_cmp_eq_u32 s89, 28
	v_add_u32_e32 v149, s65, v140
	v_add_u32_e32 v154, s65, v144
	s_cselect_b32 s37, s17, s35
	s_cselect_b32 s36, s76, s34
	ds_read_b128 v[150:153], v149
	ds_read_b128 v[154:157], v154
	v_add_u32_e32 v149, s1, v140
	s_cselect_b32 s35, s15, s88
	s_cselect_b32 s34, s77, s84
	s_add_i32 s94, 0, 0x14000
	v_add_u32_e32 v158, s1, v144
	ds_read_b128 v[166:169], v149
	ds_read_b128 v[170:173], v158
	v_add_u32_e32 v149, s94, v140
	v_add_u32_e32 v158, s94, v144
	ds_read_b128 v[174:177], v149
	ds_read_b128 v[178:181], v158
	v_add_u32_e32 v149, s86, v140
	v_add_u32_e32 v158, s86, v144
	ds_read_b128 v[182:185], v149
	ds_read_b128 v[186:189], v158
	v_lshl_add_u64 v[158:159], s[30:31], 0, v[136:137]
	s_add_i32 m0, s47, 0xc000
	ds_read_b128 v[190:193], v145
	ds_read_b128 v[194:197], v145 offset:2048
	ds_read_b128 v[198:201], v146
	ds_read_b128 v[202:205], v146 offset:2048
	ds_read_b128 v[206:209], v145 offset:4096
	ds_read_b128 v[210:213], v145 offset:6144
	ds_read_b128 v[214:217], v146 offset:4096
	ds_read_b128 v[226:229], v146 offset:6144
	global_load_lds_dwordx4 v[158:159], off
	v_lshl_add_u64 v[158:159], s[30:31], 0, v[138:139]
	s_add_i32 m0, s47, 0xe000
	s_nop 0
	global_load_lds_dwordx4 v[158:159], off
	s_waitcnt vmcnt(8)
	s_waitcnt lgkmcnt(0)
	s_barrier
	s_setprio 1
	s_waitcnt lgkmcnt(0)
	v_mfma_f32_16x16x32_bf16 v[124:127], v[150:153], v[190:193], 0
	v_mfma_f32_16x16x32_bf16 v[120:123], v[166:169], v[190:193], 0
	v_mfma_f32_16x16x32_bf16 v[116:119], v[150:153], v[194:197], 0
	v_mfma_f32_16x16x32_bf16 v[112:115], v[166:169], v[194:197], 0
	v_mfma_f32_16x16x32_bf16 v[100:103], v[150:153], v[206:209], 0
	v_mfma_f32_16x16x32_bf16 v[96:99], v[166:169], v[206:209], 0
	v_mfma_f32_16x16x32_bf16 v[84:87], v[150:153], v[210:213], 0
	v_mfma_f32_16x16x32_bf16 v[76:79], v[166:169], v[210:213], 0
	v_mfma_f32_16x16x32_bf16 v[124:127], v[154:157], v[198:201], v[124:127]
	v_mfma_f32_16x16x32_bf16 v[120:123], v[170:173], v[198:201], v[120:123]
	v_mfma_f32_16x16x32_bf16 v[116:119], v[154:157], v[202:205], v[116:119]
	v_mfma_f32_16x16x32_bf16 v[112:115], v[170:173], v[202:205], v[112:115]
	v_mfma_f32_16x16x32_bf16 v[100:103], v[154:157], v[214:217], v[100:103]
	v_mfma_f32_16x16x32_bf16 v[96:99], v[170:173], v[214:217], v[96:99]
	v_mfma_f32_16x16x32_bf16 v[84:87], v[154:157], v[226:229], v[84:87]
	v_mfma_f32_16x16x32_bf16 v[76:79], v[170:173], v[226:229], v[76:79]
	s_setprio 0
	s_setprio 1
	v_mfma_f32_16x16x32_bf16 v[108:111], v[174:177], v[190:193], 0
	v_mfma_f32_16x16x32_bf16 v[104:107], v[182:185], v[190:193], 0
	v_mfma_f32_16x16x32_bf16 v[92:95], v[174:177], v[194:197], 0
	v_mfma_f32_16x16x32_bf16 v[88:91], v[182:185], v[194:197], 0
	v_mfma_f32_16x16x32_bf16 v[80:83], v[174:177], v[206:209], 0
	v_mfma_f32_16x16x32_bf16 v[72:75], v[182:185], v[206:209], 0
	v_mfma_f32_16x16x32_bf16 v[68:71], v[174:177], v[210:213], 0
	v_mfma_f32_16x16x32_bf16 v[64:67], v[182:185], v[210:213], 0
	v_mfma_f32_16x16x32_bf16 v[108:111], v[178:181], v[198:201], v[108:111]
	v_mfma_f32_16x16x32_bf16 v[104:107], v[186:189], v[198:201], v[104:107]
	v_mfma_f32_16x16x32_bf16 v[92:95], v[178:181], v[202:205], v[92:95]
	v_mfma_f32_16x16x32_bf16 v[88:91], v[186:189], v[202:205], v[88:91]
	v_mfma_f32_16x16x32_bf16 v[80:83], v[178:181], v[214:217], v[80:83]
	v_mfma_f32_16x16x32_bf16 v[72:75], v[186:189], v[214:217], v[72:75]
	v_mfma_f32_16x16x32_bf16 v[68:71], v[178:181], v[226:229], v[68:71]
	v_mfma_f32_16x16x32_bf16 v[64:67], v[186:189], v[226:229], v[64:67]
	s_setprio 0
	s_barrier
	s_add_i32 s65, s65, s46
	v_lshl_add_u64 v[158:159], s[34:35], 0, v[132:133]
	s_mov_b32 m0, s65
	ds_read_b128 v[190:193], v145 offset:16384
	ds_read_b128 v[194:197], v145 offset:18432
	ds_read_b128 v[198:201], v146 offset:16384
	ds_read_b128 v[202:205], v146 offset:18432
	ds_read_b128 v[206:209], v145 offset:20480
	ds_read_b128 v[210:213], v145 offset:22528
	ds_read_b128 v[214:217], v146 offset:20480
	ds_read_b128 v[226:229], v146 offset:22528
	global_load_lds_dwordx4 v[158:159], off
	s_add_i32 m0, s65, 0x2000
	s_add_u32 s90, s34, 0x20000
	v_lshl_add_u64 v[218:219], s[34:35], 0, v[128:129]
	s_addc_u32 s91, s35, 0
	s_add_i32 s65, s94, s46
	global_load_lds_dwordx4 v[218:219], off
	v_lshl_add_u64 v[230:231], s[90:91], 0, v[132:133]
	s_mov_b32 m0, s65
	v_lshl_add_u64 v[232:233], s[36:37], 0, v[130:131]
	global_load_lds_dwordx4 v[230:231], off
	v_lshl_add_u64 v[230:231], s[90:91], 0, v[128:129]
	s_add_i32 m0, s65, 0x2000
	s_nop 0
	global_load_lds_dwordx4 v[230:231], off
	v_lshl_add_u64 v[230:231], s[36:37], 0, v[134:135]
	s_mov_b32 m0, s47
	s_nop 0
	global_load_lds_dwordx4 v[230:231], off
	s_mov_b32 m0, s56
	s_nop 0
	global_load_lds_dwordx4 v[232:233], off
	s_waitcnt vmcnt(8)
	s_waitcnt lgkmcnt(0)
	s_barrier
	s_setprio 1
	s_waitcnt lgkmcnt(0)
	v_mfma_f32_16x16x32_bf16 v[60:63], v[150:153], v[190:193], 0
	v_mfma_f32_16x16x32_bf16 v[56:59], v[166:169], v[190:193], 0
	v_mfma_f32_16x16x32_bf16 v[52:55], v[150:153], v[194:197], 0
	v_mfma_f32_16x16x32_bf16 v[44:47], v[166:169], v[194:197], 0
	v_mfma_f32_16x16x32_bf16 v[36:39], v[150:153], v[206:209], 0
	v_mfma_f32_16x16x32_bf16 v[28:31], v[166:169], v[206:209], 0
	v_mfma_f32_16x16x32_bf16 v[20:23], v[150:153], v[210:213], 0
	v_mfma_f32_16x16x32_bf16 v[12:15], v[166:169], v[210:213], 0
	v_mfma_f32_16x16x32_bf16 v[60:63], v[154:157], v[198:201], v[60:63]
	v_mfma_f32_16x16x32_bf16 v[56:59], v[170:173], v[198:201], v[56:59]
	v_mfma_f32_16x16x32_bf16 v[52:55], v[154:157], v[202:205], v[52:55]
	v_mfma_f32_16x16x32_bf16 v[44:47], v[170:173], v[202:205], v[44:47]
	v_mfma_f32_16x16x32_bf16 v[36:39], v[154:157], v[214:217], v[36:39]
	v_mfma_f32_16x16x32_bf16 v[28:31], v[170:173], v[214:217], v[28:31]
	v_mfma_f32_16x16x32_bf16 v[20:23], v[154:157], v[226:229], v[20:23]
	v_mfma_f32_16x16x32_bf16 v[12:15], v[170:173], v[226:229], v[12:15]
	s_setprio 0
	s_setprio 1
	v_mfma_f32_16x16x32_bf16 v[48:51], v[174:177], v[190:193], 0
	v_mfma_f32_16x16x32_bf16 v[40:43], v[182:185], v[190:193], 0
	v_mfma_f32_16x16x32_bf16 v[32:35], v[174:177], v[194:197], 0
	v_mfma_f32_16x16x32_bf16 v[24:27], v[182:185], v[194:197], 0
	v_mfma_f32_16x16x32_bf16 v[16:19], v[174:177], v[206:209], 0
	v_mfma_f32_16x16x32_bf16 v[8:11], v[182:185], v[206:209], 0
	v_mfma_f32_16x16x32_bf16 v[4:7], v[174:177], v[210:213], 0
	v_mfma_f32_16x16x32_bf16 v[0:3], v[182:185], v[210:213], 0
	v_mfma_f32_16x16x32_bf16 v[48:51], v[178:181], v[198:201], v[48:51]
	v_mfma_f32_16x16x32_bf16 v[40:43], v[186:189], v[198:201], v[40:43]
	v_mfma_f32_16x16x32_bf16 v[32:35], v[178:181], v[202:205], v[32:35]
	v_mfma_f32_16x16x32_bf16 v[24:27], v[186:189], v[202:205], v[24:27]
	v_mfma_f32_16x16x32_bf16 v[16:19], v[178:181], v[214:217], v[16:19]
	v_mfma_f32_16x16x32_bf16 v[8:11], v[186:189], v[214:217], v[8:11]
	v_mfma_f32_16x16x32_bf16 v[4:7], v[178:181], v[226:229], v[4:7]
	v_mfma_f32_16x16x32_bf16 v[0:3], v[186:189], v[226:229], v[0:3]
	s_setprio 0
	s_barrier
	s_add_i32 s65, 0, 0x18000
	v_add_u32_e32 v149, s65, v140
	v_add_u32_e32 v154, s65, v144
	ds_read_b128 v[150:153], v149
	ds_read_b128 v[154:157], v154
	v_add_u32_e32 v149, s87, v140
	s_add_i32 s90, 0, 0x1c000
	v_add_u32_e32 v162, s87, v144
	ds_read_b128 v[166:169], v149
	ds_read_b128 v[170:173], v162
	v_add_u32_e32 v149, s90, v140
	v_add_u32_e32 v162, s90, v144
	ds_read_b128 v[174:177], v149
	ds_read_b128 v[178:181], v162
	v_add_u32_e32 v149, s2, v140
	v_add_u32_e32 v162, s2, v144
	ds_read_b128 v[182:185], v149
	ds_read_b128 v[186:189], v162
	s_add_u32 s36, s36, 0x80000
	s_addc_u32 s37, s37, 0
	s_mov_b32 m0, s57
	v_lshl_add_u64 v[234:235], s[36:37], 0, v[134:135]
	ds_read_b128 v[190:193], v145 offset:32768
	ds_read_b128 v[194:197], v145 offset:34816
	ds_read_b128 v[198:201], v146 offset:32768
	ds_read_b128 v[202:205], v146 offset:34816
	ds_read_b128 v[206:209], v145 offset:36864
	ds_read_b128 v[210:213], v145 offset:38912
	ds_read_b128 v[214:217], v146 offset:36864
	ds_read_b128 v[226:229], v146 offset:38912
	global_load_lds_dwordx4 v[234:235], off
	v_lshl_add_u64 v[234:235], s[36:37], 0, v[130:131]
	s_mov_b32 m0, s58
	s_nop 0
	global_load_lds_dwordx4 v[234:235], off
	s_waitcnt vmcnt(8)
	s_waitcnt lgkmcnt(0)
	s_barrier
	s_setprio 1
	s_waitcnt lgkmcnt(0)
	v_mfma_f32_16x16x32_bf16 v[124:127], v[150:153], v[190:193], v[124:127]
	v_mfma_f32_16x16x32_bf16 v[120:123], v[166:169], v[190:193], v[120:123]
	v_mfma_f32_16x16x32_bf16 v[116:119], v[150:153], v[194:197], v[116:119]
	v_mfma_f32_16x16x32_bf16 v[112:115], v[166:169], v[194:197], v[112:115]
	v_mfma_f32_16x16x32_bf16 v[100:103], v[150:153], v[206:209], v[100:103]
	v_mfma_f32_16x16x32_bf16 v[96:99], v[166:169], v[206:209], v[96:99]
	v_mfma_f32_16x16x32_bf16 v[84:87], v[150:153], v[210:213], v[84:87]
	v_mfma_f32_16x16x32_bf16 v[76:79], v[166:169], v[210:213], v[76:79]
	v_mfma_f32_16x16x32_bf16 v[124:127], v[154:157], v[198:201], v[124:127]
	v_mfma_f32_16x16x32_bf16 v[120:123], v[170:173], v[198:201], v[120:123]
	v_mfma_f32_16x16x32_bf16 v[116:119], v[154:157], v[202:205], v[116:119]
	v_mfma_f32_16x16x32_bf16 v[112:115], v[170:173], v[202:205], v[112:115]
	v_mfma_f32_16x16x32_bf16 v[100:103], v[154:157], v[214:217], v[100:103]
	v_mfma_f32_16x16x32_bf16 v[96:99], v[170:173], v[214:217], v[96:99]
	v_mfma_f32_16x16x32_bf16 v[84:87], v[154:157], v[226:229], v[84:87]
	v_mfma_f32_16x16x32_bf16 v[76:79], v[170:173], v[226:229], v[76:79]
	s_setprio 0
	s_setprio 1
	v_mfma_f32_16x16x32_bf16 v[108:111], v[174:177], v[190:193], v[108:111]
	v_mfma_f32_16x16x32_bf16 v[104:107], v[182:185], v[190:193], v[104:107]
	v_mfma_f32_16x16x32_bf16 v[92:95], v[174:177], v[194:197], v[92:95]
	v_mfma_f32_16x16x32_bf16 v[88:91], v[182:185], v[194:197], v[88:91]
	v_mfma_f32_16x16x32_bf16 v[80:83], v[174:177], v[206:209], v[80:83]
	v_mfma_f32_16x16x32_bf16 v[72:75], v[182:185], v[206:209], v[72:75]
	v_mfma_f32_16x16x32_bf16 v[68:71], v[174:177], v[210:213], v[68:71]
	v_mfma_f32_16x16x32_bf16 v[64:67], v[182:185], v[210:213], v[64:67]
	v_mfma_f32_16x16x32_bf16 v[108:111], v[178:181], v[198:201], v[108:111]
	v_mfma_f32_16x16x32_bf16 v[104:107], v[186:189], v[198:201], v[104:107]
	v_mfma_f32_16x16x32_bf16 v[92:95], v[178:181], v[202:205], v[92:95]
	v_mfma_f32_16x16x32_bf16 v[88:91], v[186:189], v[202:205], v[88:91]
	v_mfma_f32_16x16x32_bf16 v[80:83], v[178:181], v[214:217], v[80:83]
	v_mfma_f32_16x16x32_bf16 v[72:75], v[186:189], v[214:217], v[72:75]
	v_mfma_f32_16x16x32_bf16 v[68:71], v[178:181], v[226:229], v[68:71]
	v_mfma_f32_16x16x32_bf16 v[64:67], v[186:189], v[226:229], v[64:67]
	s_setprio 0
	s_barrier
	s_add_i32 s36, s65, s46
	v_lshl_add_u64 v[158:159], v[158:159], 0, s[54:55]
	s_mov_b32 m0, s36
	ds_read_b128 v[190:193], v145 offset:49152
	ds_read_b128 v[194:197], v145 offset:51200
	ds_read_b128 v[198:201], v146 offset:49152
	ds_read_b128 v[202:205], v146 offset:51200
	ds_read_b128 v[206:209], v145 offset:53248
	ds_read_b128 v[210:213], v145 offset:55296
	ds_read_b128 v[214:217], v146 offset:53248
	ds_read_b128 v[226:229], v146 offset:55296
	global_load_lds_dwordx4 v[158:159], off
	s_add_i32 m0, s36, 0x2000
	s_add_u32 s34, s34, 0x20080
	v_lshl_add_u64 v[158:159], v[218:219], 0, s[54:55]
	s_addc_u32 s35, s35, 0
	s_add_i32 s36, s90, s46
	global_load_lds_dwordx4 v[158:159], off
	v_lshl_add_u64 v[158:159], s[34:35], 0, v[132:133]
	s_mov_b32 m0, s36
	s_nop 0
	global_load_lds_dwordx4 v[158:159], off
	v_lshl_add_u64 v[158:159], s[34:35], 0, v[128:129]
	s_add_i32 m0, s36, 0x2000
	s_nop 0
	global_load_lds_dwordx4 v[158:159], off
	v_lshl_add_u64 v[158:159], v[230:231], 0, s[54:55]
	s_mov_b32 m0, s59
	s_nop 0
	global_load_lds_dwordx4 v[158:159], off
	v_lshl_add_u64 v[158:159], v[232:233], 0, s[54:55]
	s_mov_b32 m0, s70
	s_nop 0
	global_load_lds_dwordx4 v[158:159], off
	s_waitcnt vmcnt(8)
	s_waitcnt lgkmcnt(0)
	s_barrier
	s_setprio 1
	s_waitcnt lgkmcnt(0)
	v_mfma_f32_16x16x32_bf16 v[60:63], v[150:153], v[190:193], v[60:63]
	v_mfma_f32_16x16x32_bf16 v[56:59], v[166:169], v[190:193], v[56:59]
	v_mfma_f32_16x16x32_bf16 v[52:55], v[150:153], v[194:197], v[52:55]
	v_mfma_f32_16x16x32_bf16 v[44:47], v[166:169], v[194:197], v[44:47]
	v_mfma_f32_16x16x32_bf16 v[36:39], v[150:153], v[206:209], v[36:39]
	v_mfma_f32_16x16x32_bf16 v[28:31], v[166:169], v[206:209], v[28:31]
	v_mfma_f32_16x16x32_bf16 v[20:23], v[150:153], v[210:213], v[20:23]
	v_mfma_f32_16x16x32_bf16 v[12:15], v[166:169], v[210:213], v[12:15]
	v_mfma_f32_16x16x32_bf16 v[60:63], v[154:157], v[198:201], v[60:63]
	v_mfma_f32_16x16x32_bf16 v[56:59], v[170:173], v[198:201], v[56:59]
	v_mfma_f32_16x16x32_bf16 v[52:55], v[154:157], v[202:205], v[52:55]
	v_mfma_f32_16x16x32_bf16 v[44:47], v[170:173], v[202:205], v[44:47]
	v_mfma_f32_16x16x32_bf16 v[36:39], v[154:157], v[214:217], v[36:39]
	v_mfma_f32_16x16x32_bf16 v[28:31], v[170:173], v[214:217], v[28:31]
	v_mfma_f32_16x16x32_bf16 v[20:23], v[154:157], v[226:229], v[20:23]
	v_mfma_f32_16x16x32_bf16 v[12:15], v[170:173], v[226:229], v[12:15]
	s_setprio 0
	s_setprio 1
	v_mfma_f32_16x16x32_bf16 v[48:51], v[174:177], v[190:193], v[48:51]
	v_mfma_f32_16x16x32_bf16 v[40:43], v[182:185], v[190:193], v[40:43]
	v_mfma_f32_16x16x32_bf16 v[32:35], v[174:177], v[194:197], v[32:35]
	v_mfma_f32_16x16x32_bf16 v[24:27], v[182:185], v[194:197], v[24:27]
	v_mfma_f32_16x16x32_bf16 v[16:19], v[174:177], v[206:209], v[16:19]
	v_mfma_f32_16x16x32_bf16 v[8:11], v[182:185], v[206:209], v[8:11]
	v_mfma_f32_16x16x32_bf16 v[4:7], v[174:177], v[210:213], v[4:7]
	v_mfma_f32_16x16x32_bf16 v[0:3], v[182:185], v[210:213], v[0:3]
	v_mfma_f32_16x16x32_bf16 v[48:51], v[178:181], v[198:201], v[48:51]
	v_mfma_f32_16x16x32_bf16 v[40:43], v[186:189], v[198:201], v[40:43]
	v_mfma_f32_16x16x32_bf16 v[32:35], v[178:181], v[202:205], v[32:35]
	v_mfma_f32_16x16x32_bf16 v[24:27], v[186:189], v[202:205], v[24:27]
	v_mfma_f32_16x16x32_bf16 v[16:19], v[178:181], v[214:217], v[16:19]
	v_mfma_f32_16x16x32_bf16 v[8:11], v[186:189], v[214:217], v[8:11]
	v_mfma_f32_16x16x32_bf16 v[4:7], v[178:181], v[226:229], v[4:7]
	v_mfma_f32_16x16x32_bf16 v[0:3], v[186:189], v[226:229], v[0:3]
	s_setprio 0
	s_barrier
	s_add_i32 s89, s89, 2
	s_add_u32 s30, s30, 0x100
	s_addc_u32 s31, s31, 0
	s_add_u32 s84, s84, 0x100
	s_addc_u32 s88, s88, 0
	s_cmp_gt_u32 s89, 29
	s_cbranch_scc1 .Lepi_501

.Lepi_501:
	s_and_b64 vcc, exec, s[12:13]
	s_cbranch_vccz .LBB0_504
	s_barrier

.LBB0_556:
	s_ashr_i32 s13, s12, 31
	s_lshl_b64 s[14:15], s[12:13], 20
	s_add_u32 s14, s38, s14
	s_addc_u32 s15, s39, s15
	s_and_b64 s[16:17], s[6:7], exec
	s_cselect_b32 s13, s15, s19
	s_cselect_b32 s70, s14, s18
	s_ashr_i32 s11, s10, 31
	s_lshl_b64 s[16:17], s[10:11], 20
	s_add_u32 s16, s34, s16
	s_addc_u32 s17, s35, s17
	s_and_b64 s[30:31], s[6:7], exec
	s_cselect_b32 s11, s17, s21
	s_cselect_b32 s71, s16, s20
	s_add_u32 s18, s18, 0x80080
	s_addc_u32 s19, s19, 0
	s_add_u32 s72, s20, 0x100
	s_addc_u32 s73, s21, 0
	s_mov_b32 s76, -2
	s_add_u32 s20, s18, 0xfff80080
	s_addc_u32 s21, s19, -1
	s_add_i32 s65, 0, 0x10000
	s_cmp_eq_u32 s76, 28
	v_add_u32_e32 v145, s65, v136
	v_add_u32_e32 v150, s65, v140
	s_cselect_b32 s31, s13, s21
	s_cselect_b32 s30, s70, s20
	ds_read_b128 v[146:149], v145
	ds_read_b128 v[150:153], v150
	v_add_u32_e32 v145, s1, v136
	s_cselect_b32 s21, s11, s73
	s_cselect_b32 s20, s71, s72
	s_add_i32 s77, 0, 0x14000
	v_add_u32_e32 v158, s1, v140
	ds_read_b128 v[154:157], v145
	ds_read_b128 v[166:169], v158
	v_add_u32_e32 v145, s77, v136
	v_add_u32_e32 v158, s77, v140
	ds_read_b128 v[170:173], v145
	ds_read_b128 v[174:177], v158
	v_add_u32_e32 v145, s86, v136
	v_add_u32_e32 v158, s86, v140
	ds_read_b128 v[178:181], v145
	ds_read_b128 v[182:185], v158
	v_lshl_add_u64 v[158:159], s[18:19], 0, v[132:133]
	s_add_i32 m0, s37, 0xc000
	ds_read_b128 v[186:189], v141
	ds_read_b128 v[190:193], v141 offset:2048
	ds_read_b128 v[194:197], v142
	ds_read_b128 v[198:201], v142 offset:2048
	ds_read_b128 v[202:205], v141 offset:4096
	ds_read_b128 v[206:209], v141 offset:6144
	ds_read_b128 v[210:213], v142 offset:4096
	ds_read_b128 v[214:217], v142 offset:6144
	global_load_lds_dwordx4 v[158:159], off
	v_lshl_add_u64 v[158:159], s[18:19], 0, v[134:135]
	s_add_i32 m0, s37, 0xe000
	s_nop 0
	global_load_lds_dwordx4 v[158:159], off
	s_waitcnt vmcnt(8)
	s_waitcnt lgkmcnt(0)
	s_barrier
	s_setprio 1
	s_waitcnt lgkmcnt(0)
	v_mfma_f32_16x16x32_bf16 v[124:127], v[146:149], v[186:189], 0
	v_mfma_f32_16x16x32_bf16 v[120:123], v[154:157], v[186:189], 0
	v_mfma_f32_16x16x32_bf16 v[116:119], v[146:149], v[190:193], 0
	v_mfma_f32_16x16x32_bf16 v[112:115], v[154:157], v[190:193], 0
	v_mfma_f32_16x16x32_bf16 v[100:103], v[146:149], v[202:205], 0
	v_mfma_f32_16x16x32_bf16 v[96:99], v[154:157], v[202:205], 0
	v_mfma_f32_16x16x32_bf16 v[84:87], v[146:149], v[206:209], 0
	v_mfma_f32_16x16x32_bf16 v[80:83], v[154:157], v[206:209], 0
	v_mfma_f32_16x16x32_bf16 v[124:127], v[150:153], v[194:197], v[124:127]
	v_mfma_f32_16x16x32_bf16 v[120:123], v[166:169], v[194:197], v[120:123]
	v_mfma_f32_16x16x32_bf16 v[116:119], v[150:153], v[198:201], v[116:119]
	v_mfma_f32_16x16x32_bf16 v[112:115], v[166:169], v[198:201], v[112:115]
	v_mfma_f32_16x16x32_bf16 v[100:103], v[150:153], v[210:213], v[100:103]
	v_mfma_f32_16x16x32_bf16 v[96:99], v[166:169], v[210:213], v[96:99]
	v_mfma_f32_16x16x32_bf16 v[84:87], v[150:153], v[214:217], v[84:87]
	v_mfma_f32_16x16x32_bf16 v[80:83], v[166:169], v[214:217], v[80:83]
	s_setprio 0
	s_setprio 1
	v_mfma_f32_16x16x32_bf16 v[108:111], v[170:173], v[186:189], 0
	v_mfma_f32_16x16x32_bf16 v[104:107], v[178:181], v[186:189], 0
	v_mfma_f32_16x16x32_bf16 v[92:95], v[170:173], v[190:193], 0
	v_mfma_f32_16x16x32_bf16 v[88:91], v[178:181], v[190:193], 0
	v_mfma_f32_16x16x32_bf16 v[76:79], v[170:173], v[202:205], 0
	v_mfma_f32_16x16x32_bf16 v[72:75], v[178:181], v[202:205], 0
	v_mfma_f32_16x16x32_bf16 v[68:71], v[170:173], v[206:209], 0
	v_mfma_f32_16x16x32_bf16 v[64:67], v[178:181], v[206:209], 0
	v_mfma_f32_16x16x32_bf16 v[108:111], v[174:177], v[194:197], v[108:111]
	v_mfma_f32_16x16x32_bf16 v[104:107], v[182:185], v[194:197], v[104:107]
	v_mfma_f32_16x16x32_bf16 v[92:95], v[174:177], v[198:201], v[92:95]
	v_mfma_f32_16x16x32_bf16 v[88:91], v[182:185], v[198:201], v[88:91]
	v_mfma_f32_16x16x32_bf16 v[76:79], v[174:177], v[210:213], v[76:79]
	v_mfma_f32_16x16x32_bf16 v[72:75], v[182:185], v[210:213], v[72:75]
	v_mfma_f32_16x16x32_bf16 v[68:71], v[174:177], v[214:217], v[68:71]
	v_mfma_f32_16x16x32_bf16 v[64:67], v[182:185], v[214:217], v[64:67]
	s_setprio 0
	s_barrier
	s_add_i32 s65, s65, s36
	v_lshl_add_u64 v[158:159], s[20:21], 0, v[130:131]
	s_mov_b32 m0, s65
	ds_read_b128 v[186:189], v141 offset:16384
	ds_read_b128 v[190:193], v141 offset:18432
	ds_read_b128 v[194:197], v142 offset:16384
	ds_read_b128 v[198:201], v142 offset:18432
	ds_read_b128 v[202:205], v141 offset:20480
	ds_read_b128 v[206:209], v141 offset:22528
	ds_read_b128 v[210:213], v142 offset:20480
	ds_read_b128 v[214:217], v142 offset:22528
	global_load_lds_dwordx4 v[158:159], off
	s_add_i32 m0, s65, 0x2000
	s_add_u32 s88, s20, 0x80000
	v_lshl_add_u64 v[218:219], s[20:21], 0, v[128:129]
	s_addc_u32 s89, s21, 0
	s_add_i32 s65, s77, s36
	global_load_lds_dwordx4 v[218:219], off
	v_lshl_add_u64 v[226:227], s[88:89], 0, v[130:131]
	s_mov_b32 m0, s65
	v_lshl_add_u64 v[228:229], s[30:31], 0, v[128:129]
	global_load_lds_dwordx4 v[226:227], off
	v_lshl_add_u64 v[226:227], s[88:89], 0, v[128:129]
	s_add_i32 m0, s65, 0x2000
	s_nop 0
	global_load_lds_dwordx4 v[226:227], off
	v_lshl_add_u64 v[226:227], s[30:31], 0, v[130:131]
	s_mov_b32 m0, s37
	s_nop 0
	global_load_lds_dwordx4 v[226:227], off
	s_mov_b32 m0, s41
	s_nop 0
	global_load_lds_dwordx4 v[228:229], off
	s_waitcnt vmcnt(8)
	s_waitcnt lgkmcnt(0)
	s_barrier
	s_setprio 1
	s_waitcnt lgkmcnt(0)
	v_mfma_f32_16x16x32_bf16 v[60:63], v[146:149], v[186:189], 0
	v_mfma_f32_16x16x32_bf16 v[56:59], v[154:157], v[186:189], 0
	v_mfma_f32_16x16x32_bf16 v[52:55], v[146:149], v[190:193], 0
	v_mfma_f32_16x16x32_bf16 v[48:51], v[154:157], v[190:193], 0
	v_mfma_f32_16x16x32_bf16 v[36:39], v[146:149], v[202:205], 0
	v_mfma_f32_16x16x32_bf16 v[32:35], v[154:157], v[202:205], 0
	v_mfma_f32_16x16x32_bf16 v[20:23], v[146:149], v[206:209], 0
	v_mfma_f32_16x16x32_bf16 v[16:19], v[154:157], v[206:209], 0
	v_mfma_f32_16x16x32_bf16 v[60:63], v[150:153], v[194:197], v[60:63]
	v_mfma_f32_16x16x32_bf16 v[56:59], v[166:169], v[194:197], v[56:59]
	v_mfma_f32_16x16x32_bf16 v[52:55], v[150:153], v[198:201], v[52:55]
	v_mfma_f32_16x16x32_bf16 v[48:51], v[166:169], v[198:201], v[48:51]
	v_mfma_f32_16x16x32_bf16 v[36:39], v[150:153], v[210:213], v[36:39]
	v_mfma_f32_16x16x32_bf16 v[32:35], v[166:169], v[210:213], v[32:35]
	v_mfma_f32_16x16x32_bf16 v[20:23], v[150:153], v[214:217], v[20:23]
	v_mfma_f32_16x16x32_bf16 v[16:19], v[166:169], v[214:217], v[16:19]
	s_setprio 0
	s_setprio 1
	v_mfma_f32_16x16x32_bf16 v[44:47], v[170:173], v[186:189], 0
	v_mfma_f32_16x16x32_bf16 v[40:43], v[178:181], v[186:189], 0
	v_mfma_f32_16x16x32_bf16 v[28:31], v[170:173], v[190:193], 0
	v_mfma_f32_16x16x32_bf16 v[24:27], v[178:181], v[190:193], 0
	v_mfma_f32_16x16x32_bf16 v[12:15], v[170:173], v[202:205], 0
	v_mfma_f32_16x16x32_bf16 v[8:11], v[178:181], v[202:205], 0
	v_mfma_f32_16x16x32_bf16 v[4:7], v[170:173], v[206:209], 0
	v_mfma_f32_16x16x32_bf16 v[0:3], v[178:181], v[206:209], 0
	v_mfma_f32_16x16x32_bf16 v[44:47], v[174:177], v[194:197], v[44:47]
	v_mfma_f32_16x16x32_bf16 v[40:43], v[182:185], v[194:197], v[40:43]
	v_mfma_f32_16x16x32_bf16 v[28:31], v[174:177], v[198:201], v[28:31]
	v_mfma_f32_16x16x32_bf16 v[24:27], v[182:185], v[198:201], v[24:27]
	v_mfma_f32_16x16x32_bf16 v[12:15], v[174:177], v[210:213], v[12:15]
	v_mfma_f32_16x16x32_bf16 v[8:11], v[182:185], v[210:213], v[8:11]
	v_mfma_f32_16x16x32_bf16 v[4:7], v[174:177], v[214:217], v[4:7]
	v_mfma_f32_16x16x32_bf16 v[0:3], v[182:185], v[214:217], v[0:3]
	s_setprio 0
	s_barrier
	s_add_i32 s65, 0, 0x18000
	v_add_u32_e32 v145, s65, v136
	v_add_u32_e32 v150, s65, v140
	ds_read_b128 v[146:149], v145
	ds_read_b128 v[150:153], v150
	v_add_u32_e32 v145, s87, v136
	s_add_i32 s77, 0, 0x1c000
	v_add_u32_e32 v162, s87, v140
	ds_read_b128 v[154:157], v145
	ds_read_b128 v[166:169], v162
	v_add_u32_e32 v145, s77, v136
	v_add_u32_e32 v162, s77, v140
	ds_read_b128 v[170:173], v145
	ds_read_b128 v[174:177], v162
	v_add_u32_e32 v145, s2, v136
	v_add_u32_e32 v162, s2, v140
	ds_read_b128 v[178:181], v145
	ds_read_b128 v[182:185], v162
	s_add_u32 s30, s30, 0x80000
	s_addc_u32 s31, s31, 0
	s_mov_b32 m0, s43
	v_lshl_add_u64 v[230:231], s[30:31], 0, v[130:131]
	ds_read_b128 v[186:189], v141 offset:32768
	ds_read_b128 v[190:193], v141 offset:34816
	ds_read_b128 v[194:197], v142 offset:32768
	ds_read_b128 v[198:201], v142 offset:34816
	ds_read_b128 v[202:205], v141 offset:36864
	ds_read_b128 v[206:209], v141 offset:38912
	ds_read_b128 v[210:213], v142 offset:36864
	ds_read_b128 v[214:217], v142 offset:38912
	global_load_lds_dwordx4 v[230:231], off
	v_lshl_add_u64 v[230:231], s[30:31], 0, v[128:129]
	s_mov_b32 m0, s46
	s_nop 0
	global_load_lds_dwordx4 v[230:231], off
	s_waitcnt vmcnt(8)
	s_waitcnt lgkmcnt(0)
	s_barrier
	s_setprio 1
	s_waitcnt lgkmcnt(0)
	v_mfma_f32_16x16x32_bf16 v[124:127], v[146:149], v[186:189], v[124:127]
	v_mfma_f32_16x16x32_bf16 v[120:123], v[154:157], v[186:189], v[120:123]
	v_mfma_f32_16x16x32_bf16 v[116:119], v[146:149], v[190:193], v[116:119]
	v_mfma_f32_16x16x32_bf16 v[112:115], v[154:157], v[190:193], v[112:115]
	v_mfma_f32_16x16x32_bf16 v[100:103], v[146:149], v[202:205], v[100:103]
	v_mfma_f32_16x16x32_bf16 v[96:99], v[154:157], v[202:205], v[96:99]
	v_mfma_f32_16x16x32_bf16 v[84:87], v[146:149], v[206:209], v[84:87]
	v_mfma_f32_16x16x32_bf16 v[80:83], v[154:157], v[206:209], v[80:83]
	v_mfma_f32_16x16x32_bf16 v[124:127], v[150:153], v[194:197], v[124:127]
	v_mfma_f32_16x16x32_bf16 v[120:123], v[166:169], v[194:197], v[120:123]
	v_mfma_f32_16x16x32_bf16 v[116:119], v[150:153], v[198:201], v[116:119]
	v_mfma_f32_16x16x32_bf16 v[112:115], v[166:169], v[198:201], v[112:115]
	v_mfma_f32_16x16x32_bf16 v[100:103], v[150:153], v[210:213], v[100:103]
	v_mfma_f32_16x16x32_bf16 v[96:99], v[166:169], v[210:213], v[96:99]
	v_mfma_f32_16x16x32_bf16 v[84:87], v[150:153], v[214:217], v[84:87]
	v_mfma_f32_16x16x32_bf16 v[80:83], v[166:169], v[214:217], v[80:83]
	s_setprio 0
	s_setprio 1
	v_mfma_f32_16x16x32_bf16 v[108:111], v[170:173], v[186:189], v[108:111]
	v_mfma_f32_16x16x32_bf16 v[104:107], v[178:181], v[186:189], v[104:107]
	v_mfma_f32_16x16x32_bf16 v[92:95], v[170:173], v[190:193], v[92:95]
	v_mfma_f32_16x16x32_bf16 v[88:91], v[178:181], v[190:193], v[88:91]
	v_mfma_f32_16x16x32_bf16 v[76:79], v[170:173], v[202:205], v[76:79]
	v_mfma_f32_16x16x32_bf16 v[72:75], v[178:181], v[202:205], v[72:75]
	v_mfma_f32_16x16x32_bf16 v[68:71], v[170:173], v[206:209], v[68:71]
	v_mfma_f32_16x16x32_bf16 v[64:67], v[178:181], v[206:209], v[64:67]
	v_mfma_f32_16x16x32_bf16 v[108:111], v[174:177], v[194:197], v[108:111]
	v_mfma_f32_16x16x32_bf16 v[104:107], v[182:185], v[194:197], v[104:107]
	v_mfma_f32_16x16x32_bf16 v[92:95], v[174:177], v[198:201], v[92:95]
	v_mfma_f32_16x16x32_bf16 v[88:91], v[182:185], v[198:201], v[88:91]
	v_mfma_f32_16x16x32_bf16 v[76:79], v[174:177], v[210:213], v[76:79]
	v_mfma_f32_16x16x32_bf16 v[72:75], v[182:185], v[210:213], v[72:75]
	v_mfma_f32_16x16x32_bf16 v[68:71], v[174:177], v[214:217], v[68:71]
	v_mfma_f32_16x16x32_bf16 v[64:67], v[182:185], v[214:217], v[64:67]
	s_setprio 0
	s_barrier
	s_add_i32 s30, s65, s36
	v_lshl_add_u64 v[158:159], v[158:159], 0, s[54:55]
	s_mov_b32 m0, s30
	ds_read_b128 v[186:189], v141 offset:49152
	ds_read_b128 v[190:193], v141 offset:51200
	ds_read_b128 v[194:197], v142 offset:49152
	ds_read_b128 v[198:201], v142 offset:51200
	ds_read_b128 v[202:205], v141 offset:53248
	ds_read_b128 v[206:209], v141 offset:55296
	ds_read_b128 v[210:213], v142 offset:53248
	ds_read_b128 v[214:217], v142 offset:55296
	global_load_lds_dwordx4 v[158:159], off
	s_add_i32 m0, s30, 0x2000
	s_add_u32 s20, s20, 0x80080
	v_lshl_add_u64 v[158:159], v[218:219], 0, s[54:55]
	s_addc_u32 s21, s21, 0
	s_add_i32 s30, s77, s36
	global_load_lds_dwordx4 v[158:159], off
	v_lshl_add_u64 v[158:159], s[20:21], 0, v[130:131]
	s_mov_b32 m0, s30
	s_nop 0
	global_load_lds_dwordx4 v[158:159], off
	v_lshl_add_u64 v[158:159], s[20:21], 0, v[128:129]
	s_add_i32 m0, s30, 0x2000
	s_nop 0
	global_load_lds_dwordx4 v[158:159], off
	v_lshl_add_u64 v[158:159], v[226:227], 0, s[54:55]
	s_mov_b32 m0, s47
	s_nop 0
	global_load_lds_dwordx4 v[158:159], off
	v_lshl_add_u64 v[158:159], v[228:229], 0, s[54:55]
	s_mov_b32 m0, s56
	s_nop 0
	global_load_lds_dwordx4 v[158:159], off
	s_waitcnt vmcnt(8)
	s_waitcnt lgkmcnt(0)
	s_barrier
	s_setprio 1
	s_waitcnt lgkmcnt(0)
	v_mfma_f32_16x16x32_bf16 v[60:63], v[146:149], v[186:189], v[60:63]
	v_mfma_f32_16x16x32_bf16 v[56:59], v[154:157], v[186:189], v[56:59]
	v_mfma_f32_16x16x32_bf16 v[52:55], v[146:149], v[190:193], v[52:55]
	v_mfma_f32_16x16x32_bf16 v[48:51], v[154:157], v[190:193], v[48:51]
	v_mfma_f32_16x16x32_bf16 v[36:39], v[146:149], v[202:205], v[36:39]
	v_mfma_f32_16x16x32_bf16 v[32:35], v[154:157], v[202:205], v[32:35]
	v_mfma_f32_16x16x32_bf16 v[20:23], v[146:149], v[206:209], v[20:23]
	v_mfma_f32_16x16x32_bf16 v[16:19], v[154:157], v[206:209], v[16:19]
	v_mfma_f32_16x16x32_bf16 v[60:63], v[150:153], v[194:197], v[60:63]
	v_mfma_f32_16x16x32_bf16 v[56:59], v[166:169], v[194:197], v[56:59]
	v_mfma_f32_16x16x32_bf16 v[52:55], v[150:153], v[198:201], v[52:55]
	v_mfma_f32_16x16x32_bf16 v[48:51], v[166:169], v[198:201], v[48:51]
	v_mfma_f32_16x16x32_bf16 v[36:39], v[150:153], v[210:213], v[36:39]
	v_mfma_f32_16x16x32_bf16 v[32:35], v[166:169], v[210:213], v[32:35]
	v_mfma_f32_16x16x32_bf16 v[20:23], v[150:153], v[214:217], v[20:23]
	v_mfma_f32_16x16x32_bf16 v[16:19], v[166:169], v[214:217], v[16:19]
	s_setprio 0
	s_setprio 1
	v_mfma_f32_16x16x32_bf16 v[44:47], v[170:173], v[186:189], v[44:47]
	v_mfma_f32_16x16x32_bf16 v[40:43], v[178:181], v[186:189], v[40:43]
	v_mfma_f32_16x16x32_bf16 v[28:31], v[170:173], v[190:193], v[28:31]
	v_mfma_f32_16x16x32_bf16 v[24:27], v[178:181], v[190:193], v[24:27]
	v_mfma_f32_16x16x32_bf16 v[12:15], v[170:173], v[202:205], v[12:15]
	v_mfma_f32_16x16x32_bf16 v[8:11], v[178:181], v[202:205], v[8:11]
	v_mfma_f32_16x16x32_bf16 v[4:7], v[170:173], v[206:209], v[4:7]
	v_mfma_f32_16x16x32_bf16 v[0:3], v[178:181], v[206:209], v[0:3]
	v_mfma_f32_16x16x32_bf16 v[44:47], v[174:177], v[194:197], v[44:47]
	v_mfma_f32_16x16x32_bf16 v[40:43], v[182:185], v[194:197], v[40:43]
	v_mfma_f32_16x16x32_bf16 v[28:31], v[174:177], v[198:201], v[28:31]
	v_mfma_f32_16x16x32_bf16 v[24:27], v[182:185], v[198:201], v[24:27]
	v_mfma_f32_16x16x32_bf16 v[12:15], v[174:177], v[210:213], v[12:15]
	v_mfma_f32_16x16x32_bf16 v[8:11], v[182:185], v[210:213], v[8:11]
	v_mfma_f32_16x16x32_bf16 v[4:7], v[174:177], v[214:217], v[4:7]
	v_mfma_f32_16x16x32_bf16 v[0:3], v[182:185], v[214:217], v[0:3]
	s_setprio 0
	s_barrier
	s_add_i32 s76, s76, 2
	s_add_u32 s18, s18, 0x100
	s_addc_u32 s19, s19, 0
	s_add_u32 s72, s72, 0x100
	s_addc_u32 s73, s73, 0
	s_cmp_gt_u32 s76, 29
	s_cbranch_scc1 .Lepi_557

.Lepi_557:
	s_and_b64 vcc, exec, s[8:9]
	s_cbranch_vccz .LBB0_560
	s_barrier

.LBB0_651:
	s_ashr_i32 s13, s12, 31
	s_lshl_b64 s[14:15], s[12:13], 18
	v_readlane_b32 s11, v254, 9
	s_add_u32 s14, s11, s14
	v_readlane_b32 s11, v254, 10
	s_addc_u32 s15, s11, s15
	s_and_b64 s[16:17], s[6:7], exec
	s_cselect_b32 s13, s15, s19
	s_cselect_b32 s36, s14, s18
	s_ashr_i32 s11, s10, 31
	s_lshl_b64 s[16:17], s[10:11], 18
	s_add_u32 s16, s41, s16
	s_addc_u32 s17, s43, s17
	s_and_b64 s[30:31], s[6:7], exec
	s_cselect_b32 s11, s17, s21
	s_cselect_b32 s37, s16, s20
	s_add_u32 s18, s18, 0x20080
	s_addc_u32 s19, s19, 0
	s_waitcnt lgkmcnt(0)
	s_add_u32 s46, s20, 0x100
	s_addc_u32 s47, s21, 0
	s_mov_b32 s56, -2
	s_add_u32 s20, s18, 0xfffe0080
	s_addc_u32 s21, s19, -1
	s_add_i32 s57, 0, 0x10000
	s_cmp_eq_u32 s56, 4
	v_add_u32_e32 v149, s57, v140
	v_add_u32_e32 v154, s57, v144
	s_cselect_b32 s31, s13, s21
	s_cselect_b32 s30, s36, s20
	ds_read_b128 v[150:153], v149
	ds_read_b128 v[154:157], v154
	v_add_u32_e32 v149, s1, v140
	s_cselect_b32 s21, s11, s47
	s_cselect_b32 s20, s37, s46
	s_add_i32 s65, 0, 0x14000
	v_add_u32_e32 v158, s1, v144
	ds_read_b128 v[166:169], v149
	ds_read_b128 v[170:173], v158
	v_add_u32_e32 v149, s65, v140
	v_add_u32_e32 v158, s65, v144
	ds_read_b128 v[174:177], v149
	ds_read_b128 v[178:181], v158
	v_add_u32_e32 v149, s86, v140
	v_add_u32_e32 v158, s86, v144
	ds_read_b128 v[182:185], v149
	ds_read_b128 v[186:189], v158
	v_lshl_add_u64 v[158:159], s[18:19], 0, v[136:137]
	s_add_i32 m0, s77, 0xc000
	ds_read_b128 v[190:193], v145
	ds_read_b128 v[194:197], v145 offset:2048
	ds_read_b128 v[198:201], v146
	ds_read_b128 v[202:205], v146 offset:2048
	ds_read_b128 v[206:209], v145 offset:4096
	ds_read_b128 v[210:213], v145 offset:6144
	ds_read_b128 v[214:217], v146 offset:4096
	ds_read_b128 v[226:229], v146 offset:6144
	global_load_lds_dwordx4 v[158:159], off
	v_lshl_add_u64 v[158:159], s[18:19], 0, v[138:139]
	s_add_i32 m0, s77, 0xe000
	s_nop 0
	global_load_lds_dwordx4 v[158:159], off
	s_waitcnt vmcnt(8)
	s_waitcnt lgkmcnt(0)
	s_barrier
	s_setprio 1
	s_waitcnt lgkmcnt(0)
	v_mfma_f32_16x16x32_bf16 v[124:127], v[150:153], v[190:193], 0
	v_mfma_f32_16x16x32_bf16 v[120:123], v[166:169], v[190:193], 0
	v_mfma_f32_16x16x32_bf16 v[116:119], v[150:153], v[194:197], 0
	v_mfma_f32_16x16x32_bf16 v[112:115], v[166:169], v[194:197], 0
	v_mfma_f32_16x16x32_bf16 v[100:103], v[150:153], v[206:209], 0
	v_mfma_f32_16x16x32_bf16 v[96:99], v[166:169], v[206:209], 0
	v_mfma_f32_16x16x32_bf16 v[84:87], v[150:153], v[210:213], 0
	v_mfma_f32_16x16x32_bf16 v[80:83], v[166:169], v[210:213], 0
	v_mfma_f32_16x16x32_bf16 v[124:127], v[154:157], v[198:201], v[124:127]
	v_mfma_f32_16x16x32_bf16 v[120:123], v[170:173], v[198:201], v[120:123]
	v_mfma_f32_16x16x32_bf16 v[116:119], v[154:157], v[202:205], v[116:119]
	v_mfma_f32_16x16x32_bf16 v[112:115], v[170:173], v[202:205], v[112:115]
	v_mfma_f32_16x16x32_bf16 v[100:103], v[154:157], v[214:217], v[100:103]
	v_mfma_f32_16x16x32_bf16 v[96:99], v[170:173], v[214:217], v[96:99]
	v_mfma_f32_16x16x32_bf16 v[84:87], v[154:157], v[226:229], v[84:87]
	v_mfma_f32_16x16x32_bf16 v[80:83], v[170:173], v[226:229], v[80:83]
	s_setprio 0
	s_setprio 1
	v_mfma_f32_16x16x32_bf16 v[108:111], v[174:177], v[190:193], 0
	v_mfma_f32_16x16x32_bf16 v[104:107], v[182:185], v[190:193], 0
	v_mfma_f32_16x16x32_bf16 v[92:95], v[174:177], v[194:197], 0
	v_mfma_f32_16x16x32_bf16 v[88:91], v[182:185], v[194:197], 0
	v_mfma_f32_16x16x32_bf16 v[76:79], v[174:177], v[206:209], 0
	v_mfma_f32_16x16x32_bf16 v[72:75], v[182:185], v[206:209], 0
	v_mfma_f32_16x16x32_bf16 v[68:71], v[174:177], v[210:213], 0
	v_mfma_f32_16x16x32_bf16 v[64:67], v[182:185], v[210:213], 0
	v_mfma_f32_16x16x32_bf16 v[108:111], v[178:181], v[198:201], v[108:111]
	v_mfma_f32_16x16x32_bf16 v[104:107], v[186:189], v[198:201], v[104:107]
	v_mfma_f32_16x16x32_bf16 v[92:95], v[178:181], v[202:205], v[92:95]
	v_mfma_f32_16x16x32_bf16 v[88:91], v[186:189], v[202:205], v[88:91]
	v_mfma_f32_16x16x32_bf16 v[76:79], v[178:181], v[214:217], v[76:79]
	v_mfma_f32_16x16x32_bf16 v[72:75], v[186:189], v[214:217], v[72:75]
	v_mfma_f32_16x16x32_bf16 v[68:71], v[178:181], v[226:229], v[68:71]
	v_mfma_f32_16x16x32_bf16 v[64:67], v[186:189], v[226:229], v[64:67]
	s_setprio 0
	s_barrier
	s_add_i32 s57, s57, s76
	v_lshl_add_u64 v[158:159], s[20:21], 0, v[132:133]
	s_mov_b32 m0, s57
	ds_read_b128 v[190:193], v145 offset:16384
	ds_read_b128 v[194:197], v145 offset:18432
	ds_read_b128 v[198:201], v146 offset:16384
	ds_read_b128 v[202:205], v146 offset:18432
	ds_read_b128 v[206:209], v145 offset:20480
	ds_read_b128 v[210:213], v145 offset:22528
	ds_read_b128 v[214:217], v146 offset:20480
	ds_read_b128 v[226:229], v146 offset:22528
	global_load_lds_dwordx4 v[158:159], off
	s_add_i32 m0, s57, 0x2000
	s_add_u32 s58, s20, 0x8000
	v_lshl_add_u64 v[218:219], s[20:21], 0, v[128:129]
	s_addc_u32 s59, s21, 0
	s_add_i32 s57, s65, s76
	global_load_lds_dwordx4 v[218:219], off
	v_lshl_add_u64 v[230:231], s[58:59], 0, v[132:133]
	s_mov_b32 m0, s57
	v_lshl_add_u64 v[232:233], s[30:31], 0, v[130:131]
	global_load_lds_dwordx4 v[230:231], off
	v_lshl_add_u64 v[230:231], s[58:59], 0, v[128:129]
	s_add_i32 m0, s57, 0x2000
	s_nop 0
	global_load_lds_dwordx4 v[230:231], off
	v_lshl_add_u64 v[230:231], s[30:31], 0, v[134:135]
	s_mov_b32 m0, s77
	s_nop 0
	global_load_lds_dwordx4 v[230:231], off
	s_mov_b32 m0, s84
	s_nop 0
	global_load_lds_dwordx4 v[232:233], off
	s_waitcnt vmcnt(8)
	s_waitcnt lgkmcnt(0)
	s_barrier
	s_setprio 1
	s_waitcnt lgkmcnt(0)
	v_mfma_f32_16x16x32_bf16 v[60:63], v[150:153], v[190:193], 0
	v_mfma_f32_16x16x32_bf16 v[56:59], v[166:169], v[190:193], 0
	v_mfma_f32_16x16x32_bf16 v[52:55], v[150:153], v[194:197], 0
	v_mfma_f32_16x16x32_bf16 v[44:47], v[166:169], v[194:197], 0
	v_mfma_f32_16x16x32_bf16 v[36:39], v[150:153], v[206:209], 0
	v_mfma_f32_16x16x32_bf16 v[28:31], v[166:169], v[206:209], 0
	v_mfma_f32_16x16x32_bf16 v[20:23], v[150:153], v[210:213], 0
	v_mfma_f32_16x16x32_bf16 v[12:15], v[166:169], v[210:213], 0
	v_mfma_f32_16x16x32_bf16 v[60:63], v[154:157], v[198:201], v[60:63]
	v_mfma_f32_16x16x32_bf16 v[56:59], v[170:173], v[198:201], v[56:59]
	v_mfma_f32_16x16x32_bf16 v[52:55], v[154:157], v[202:205], v[52:55]
	v_mfma_f32_16x16x32_bf16 v[44:47], v[170:173], v[202:205], v[44:47]
	v_mfma_f32_16x16x32_bf16 v[36:39], v[154:157], v[214:217], v[36:39]
	v_mfma_f32_16x16x32_bf16 v[28:31], v[170:173], v[214:217], v[28:31]
	v_mfma_f32_16x16x32_bf16 v[20:23], v[154:157], v[226:229], v[20:23]
	v_mfma_f32_16x16x32_bf16 v[12:15], v[170:173], v[226:229], v[12:15]
	s_setprio 0
	s_setprio 1
	v_mfma_f32_16x16x32_bf16 v[48:51], v[174:177], v[190:193], 0
	v_mfma_f32_16x16x32_bf16 v[40:43], v[182:185], v[190:193], 0
	v_mfma_f32_16x16x32_bf16 v[32:35], v[174:177], v[194:197], 0
	v_mfma_f32_16x16x32_bf16 v[24:27], v[182:185], v[194:197], 0
	v_mfma_f32_16x16x32_bf16 v[16:19], v[174:177], v[206:209], 0
	v_mfma_f32_16x16x32_bf16 v[8:11], v[182:185], v[206:209], 0
	v_mfma_f32_16x16x32_bf16 v[4:7], v[174:177], v[210:213], 0
	v_mfma_f32_16x16x32_bf16 v[0:3], v[182:185], v[210:213], 0
	v_mfma_f32_16x16x32_bf16 v[48:51], v[178:181], v[198:201], v[48:51]
	v_mfma_f32_16x16x32_bf16 v[40:43], v[186:189], v[198:201], v[40:43]
	v_mfma_f32_16x16x32_bf16 v[32:35], v[178:181], v[202:205], v[32:35]
	v_mfma_f32_16x16x32_bf16 v[24:27], v[186:189], v[202:205], v[24:27]
	v_mfma_f32_16x16x32_bf16 v[16:19], v[178:181], v[214:217], v[16:19]
	v_mfma_f32_16x16x32_bf16 v[8:11], v[186:189], v[214:217], v[8:11]
	v_mfma_f32_16x16x32_bf16 v[4:7], v[178:181], v[226:229], v[4:7]
	v_mfma_f32_16x16x32_bf16 v[0:3], v[186:189], v[226:229], v[0:3]
	s_setprio 0
	s_barrier
	s_add_i32 s57, 0, 0x18000
	v_add_u32_e32 v149, s57, v140
	v_add_u32_e32 v154, s57, v144
	ds_read_b128 v[150:153], v149
	ds_read_b128 v[154:157], v154
	v_add_u32_e32 v149, s87, v140
	s_add_i32 s58, 0, 0x1c000
	v_add_u32_e32 v162, s87, v144
	ds_read_b128 v[166:169], v149
	ds_read_b128 v[170:173], v162
	v_add_u32_e32 v149, s58, v140
	v_add_u32_e32 v162, s58, v144
	ds_read_b128 v[174:177], v149
	ds_read_b128 v[178:181], v162
	v_add_u32_e32 v149, s2, v140
	v_add_u32_e32 v162, s2, v144
	ds_read_b128 v[182:185], v149
	ds_read_b128 v[186:189], v162
	s_add_u32 s30, s30, 0x20000
	s_addc_u32 s31, s31, 0
	s_mov_b32 m0, s88
	v_lshl_add_u64 v[234:235], s[30:31], 0, v[134:135]
	ds_read_b128 v[190:193], v145 offset:32768
	ds_read_b128 v[194:197], v145 offset:34816
	ds_read_b128 v[198:201], v146 offset:32768
	ds_read_b128 v[202:205], v146 offset:34816
	ds_read_b128 v[206:209], v145 offset:36864
	ds_read_b128 v[210:213], v145 offset:38912
	ds_read_b128 v[214:217], v146 offset:36864
	ds_read_b128 v[226:229], v146 offset:38912
	global_load_lds_dwordx4 v[234:235], off
	v_lshl_add_u64 v[234:235], s[30:31], 0, v[130:131]
	s_mov_b32 m0, s89
	s_nop 0
	global_load_lds_dwordx4 v[234:235], off
	s_waitcnt vmcnt(8)
	s_waitcnt lgkmcnt(0)
	s_barrier
	s_setprio 1
	s_waitcnt lgkmcnt(0)
	v_mfma_f32_16x16x32_bf16 v[124:127], v[150:153], v[190:193], v[124:127]
	v_mfma_f32_16x16x32_bf16 v[120:123], v[166:169], v[190:193], v[120:123]
	v_mfma_f32_16x16x32_bf16 v[116:119], v[150:153], v[194:197], v[116:119]
	v_mfma_f32_16x16x32_bf16 v[112:115], v[166:169], v[194:197], v[112:115]
	v_mfma_f32_16x16x32_bf16 v[100:103], v[150:153], v[206:209], v[100:103]
	v_mfma_f32_16x16x32_bf16 v[96:99], v[166:169], v[206:209], v[96:99]
	v_mfma_f32_16x16x32_bf16 v[84:87], v[150:153], v[210:213], v[84:87]
	v_mfma_f32_16x16x32_bf16 v[80:83], v[166:169], v[210:213], v[80:83]
	v_mfma_f32_16x16x32_bf16 v[124:127], v[154:157], v[198:201], v[124:127]
	v_mfma_f32_16x16x32_bf16 v[120:123], v[170:173], v[198:201], v[120:123]
	v_mfma_f32_16x16x32_bf16 v[116:119], v[154:157], v[202:205], v[116:119]
	v_mfma_f32_16x16x32_bf16 v[112:115], v[170:173], v[202:205], v[112:115]
	v_mfma_f32_16x16x32_bf16 v[100:103], v[154:157], v[214:217], v[100:103]
	v_mfma_f32_16x16x32_bf16 v[96:99], v[170:173], v[214:217], v[96:99]
	v_mfma_f32_16x16x32_bf16 v[84:87], v[154:157], v[226:229], v[84:87]
	v_mfma_f32_16x16x32_bf16 v[80:83], v[170:173], v[226:229], v[80:83]
	s_setprio 0
	s_setprio 1
	v_mfma_f32_16x16x32_bf16 v[108:111], v[174:177], v[190:193], v[108:111]
	v_mfma_f32_16x16x32_bf16 v[104:107], v[182:185], v[190:193], v[104:107]
	v_mfma_f32_16x16x32_bf16 v[92:95], v[174:177], v[194:197], v[92:95]
	v_mfma_f32_16x16x32_bf16 v[88:91], v[182:185], v[194:197], v[88:91]
	v_mfma_f32_16x16x32_bf16 v[76:79], v[174:177], v[206:209], v[76:79]
	v_mfma_f32_16x16x32_bf16 v[72:75], v[182:185], v[206:209], v[72:75]
	v_mfma_f32_16x16x32_bf16 v[68:71], v[174:177], v[210:213], v[68:71]
	v_mfma_f32_16x16x32_bf16 v[64:67], v[182:185], v[210:213], v[64:67]
	v_mfma_f32_16x16x32_bf16 v[108:111], v[178:181], v[198:201], v[108:111]
	v_mfma_f32_16x16x32_bf16 v[104:107], v[186:189], v[198:201], v[104:107]
	v_mfma_f32_16x16x32_bf16 v[92:95], v[178:181], v[202:205], v[92:95]
	v_mfma_f32_16x16x32_bf16 v[88:91], v[186:189], v[202:205], v[88:91]
	v_mfma_f32_16x16x32_bf16 v[76:79], v[178:181], v[214:217], v[76:79]
	v_mfma_f32_16x16x32_bf16 v[72:75], v[186:189], v[214:217], v[72:75]
	v_mfma_f32_16x16x32_bf16 v[68:71], v[178:181], v[226:229], v[68:71]
	v_mfma_f32_16x16x32_bf16 v[64:67], v[186:189], v[226:229], v[64:67]
	s_setprio 0
	s_barrier
	s_add_i32 s30, s57, s76
	v_lshl_add_u64 v[158:159], v[158:159], 0, s[54:55]
	s_mov_b32 m0, s30
	ds_read_b128 v[190:193], v145 offset:49152
	ds_read_b128 v[194:197], v145 offset:51200
	ds_read_b128 v[198:201], v146 offset:49152
	ds_read_b128 v[202:205], v146 offset:51200
	ds_read_b128 v[206:209], v145 offset:53248
	ds_read_b128 v[210:213], v145 offset:55296
	ds_read_b128 v[214:217], v146 offset:53248
	ds_read_b128 v[226:229], v146 offset:55296
	global_load_lds_dwordx4 v[158:159], off
	s_add_i32 m0, s30, 0x2000
	s_add_u32 s20, s20, 0x8080
	v_lshl_add_u64 v[158:159], v[218:219], 0, s[54:55]
	s_addc_u32 s21, s21, 0
	s_add_i32 s30, s58, s76
	global_load_lds_dwordx4 v[158:159], off
	v_lshl_add_u64 v[158:159], s[20:21], 0, v[132:133]
	s_mov_b32 m0, s30
	s_nop 0
	global_load_lds_dwordx4 v[158:159], off
	v_lshl_add_u64 v[158:159], s[20:21], 0, v[128:129]
	s_add_i32 m0, s30, 0x2000
	s_nop 0
	global_load_lds_dwordx4 v[158:159], off
	v_lshl_add_u64 v[158:159], v[230:231], 0, s[54:55]
	s_mov_b32 m0, s90
	s_nop 0
	global_load_lds_dwordx4 v[158:159], off
	v_lshl_add_u64 v[158:159], v[232:233], 0, s[54:55]
	s_mov_b32 m0, s91
	s_nop 0
	global_load_lds_dwordx4 v[158:159], off
	s_waitcnt vmcnt(8)
	s_waitcnt lgkmcnt(0)
	s_barrier
	s_setprio 1
	s_waitcnt lgkmcnt(0)
	v_mfma_f32_16x16x32_bf16 v[60:63], v[150:153], v[190:193], v[60:63]
	v_mfma_f32_16x16x32_bf16 v[56:59], v[166:169], v[190:193], v[56:59]
	v_mfma_f32_16x16x32_bf16 v[52:55], v[150:153], v[194:197], v[52:55]
	v_mfma_f32_16x16x32_bf16 v[44:47], v[166:169], v[194:197], v[44:47]
	v_mfma_f32_16x16x32_bf16 v[36:39], v[150:153], v[206:209], v[36:39]
	v_mfma_f32_16x16x32_bf16 v[28:31], v[166:169], v[206:209], v[28:31]
	v_mfma_f32_16x16x32_bf16 v[20:23], v[150:153], v[210:213], v[20:23]
	v_mfma_f32_16x16x32_bf16 v[12:15], v[166:169], v[210:213], v[12:15]
	v_mfma_f32_16x16x32_bf16 v[60:63], v[154:157], v[198:201], v[60:63]
	v_mfma_f32_16x16x32_bf16 v[56:59], v[170:173], v[198:201], v[56:59]
	v_mfma_f32_16x16x32_bf16 v[52:55], v[154:157], v[202:205], v[52:55]
	v_mfma_f32_16x16x32_bf16 v[44:47], v[170:173], v[202:205], v[44:47]
	v_mfma_f32_16x16x32_bf16 v[36:39], v[154:157], v[214:217], v[36:39]
	v_mfma_f32_16x16x32_bf16 v[28:31], v[170:173], v[214:217], v[28:31]
	v_mfma_f32_16x16x32_bf16 v[20:23], v[154:157], v[226:229], v[20:23]
	v_mfma_f32_16x16x32_bf16 v[12:15], v[170:173], v[226:229], v[12:15]
	s_setprio 0
	s_setprio 1
	v_mfma_f32_16x16x32_bf16 v[48:51], v[174:177], v[190:193], v[48:51]
	v_mfma_f32_16x16x32_bf16 v[40:43], v[182:185], v[190:193], v[40:43]
	v_mfma_f32_16x16x32_bf16 v[32:35], v[174:177], v[194:197], v[32:35]
	v_mfma_f32_16x16x32_bf16 v[24:27], v[182:185], v[194:197], v[24:27]
	v_mfma_f32_16x16x32_bf16 v[16:19], v[174:177], v[206:209], v[16:19]
	v_mfma_f32_16x16x32_bf16 v[8:11], v[182:185], v[206:209], v[8:11]
	v_mfma_f32_16x16x32_bf16 v[4:7], v[174:177], v[210:213], v[4:7]
	v_mfma_f32_16x16x32_bf16 v[0:3], v[182:185], v[210:213], v[0:3]
	v_mfma_f32_16x16x32_bf16 v[48:51], v[178:181], v[198:201], v[48:51]
	v_mfma_f32_16x16x32_bf16 v[40:43], v[186:189], v[198:201], v[40:43]
	v_mfma_f32_16x16x32_bf16 v[32:35], v[178:181], v[202:205], v[32:35]
	v_mfma_f32_16x16x32_bf16 v[24:27], v[186:189], v[202:205], v[24:27]
	v_mfma_f32_16x16x32_bf16 v[16:19], v[178:181], v[214:217], v[16:19]
	v_mfma_f32_16x16x32_bf16 v[8:11], v[186:189], v[214:217], v[8:11]
	v_mfma_f32_16x16x32_bf16 v[4:7], v[178:181], v[226:229], v[4:7]
	v_mfma_f32_16x16x32_bf16 v[0:3], v[186:189], v[226:229], v[0:3]
	s_setprio 0
	s_barrier
	s_add_i32 s56, s56, 2
	s_add_u32 s18, s18, 0x100
	s_addc_u32 s19, s19, 0
	s_add_u32 s46, s46, 0x100
	s_addc_u32 s47, s47, 0
	s_cmp_gt_u32 s56, 5
	s_cbranch_scc1 .Lepi_652

.LBB0_855:
	s_lshl_b64 s[16:17], s[12:13], 18
	s_add_u32 s16, s34, s16
	s_addc_u32 s17, s35, s17
	s_and_b64 s[30:31], s[6:7], exec
	s_cselect_b32 s13, s17, s21
	s_cselect_b32 s15, s16, s20
	s_add_u32 s18, s18, 0x200080
	s_addc_u32 s19, s19, 0
	s_add_u32 s70, s20, 0x100
	s_addc_u32 s71, s21, 0
	s_mov_b32 s72, -2
	s_add_u32 s20, s18, 0xffe00080
	s_addc_u32 s21, s19, -1
	s_add_i32 s65, 0, 0x10000
	s_cmp_eq_u32 s72, 4
	v_add_u32_e32 v149, s65, v140
	v_add_u32_e32 v154, s65, v144
	s_cselect_b32 s31, s9, s21
	s_cselect_b32 s30, s8, s20
	ds_read_b128 v[150:153], v149
	ds_read_b128 v[154:157], v154
	v_add_u32_e32 v149, s1, v140
	s_cselect_b32 s21, s13, s71
	s_cselect_b32 s20, s15, s70
	s_add_i32 s73, 0, 0x14000
	v_add_u32_e32 v158, s1, v144
	ds_read_b128 v[166:169], v149
	ds_read_b128 v[170:173], v158
	v_add_u32_e32 v149, s73, v140
	v_add_u32_e32 v158, s73, v144
	ds_read_b128 v[174:177], v149
	ds_read_b128 v[178:181], v158
	v_add_u32_e32 v149, s86, v140
	v_add_u32_e32 v158, s86, v144
	ds_read_b128 v[182:185], v149
	ds_read_b128 v[186:189], v158
	v_lshl_add_u64 v[158:159], s[18:19], 0, v[136:137]
	s_add_i32 m0, s37, 0xc000
	ds_read_b128 v[190:193], v145
	ds_read_b128 v[194:197], v145 offset:2048
	ds_read_b128 v[198:201], v146
	ds_read_b128 v[202:205], v146 offset:2048
	ds_read_b128 v[206:209], v145 offset:4096
	ds_read_b128 v[210:213], v145 offset:6144
	ds_read_b128 v[214:217], v146 offset:4096
	ds_read_b128 v[226:229], v146 offset:6144
	global_load_lds_dwordx4 v[158:159], off
	v_lshl_add_u64 v[158:159], s[18:19], 0, v[138:139]
	s_add_i32 m0, s37, 0xe000
	s_nop 0
	global_load_lds_dwordx4 v[158:159], off
	s_waitcnt vmcnt(8)
	s_waitcnt lgkmcnt(0)
	s_barrier
	s_setprio 1
	s_waitcnt lgkmcnt(0)
	v_mfma_f32_16x16x32_bf16 v[124:127], v[150:153], v[190:193], 0
	v_mfma_f32_16x16x32_bf16 v[120:123], v[166:169], v[190:193], 0
	v_mfma_f32_16x16x32_bf16 v[116:119], v[150:153], v[194:197], 0
	v_mfma_f32_16x16x32_bf16 v[112:115], v[166:169], v[194:197], 0
	v_mfma_f32_16x16x32_bf16 v[100:103], v[150:153], v[206:209], 0
	v_mfma_f32_16x16x32_bf16 v[96:99], v[166:169], v[206:209], 0
	v_mfma_f32_16x16x32_bf16 v[84:87], v[150:153], v[210:213], 0
	v_mfma_f32_16x16x32_bf16 v[76:79], v[166:169], v[210:213], 0
	v_mfma_f32_16x16x32_bf16 v[124:127], v[154:157], v[198:201], v[124:127]
	v_mfma_f32_16x16x32_bf16 v[120:123], v[170:173], v[198:201], v[120:123]
	v_mfma_f32_16x16x32_bf16 v[116:119], v[154:157], v[202:205], v[116:119]
	v_mfma_f32_16x16x32_bf16 v[112:115], v[170:173], v[202:205], v[112:115]
	v_mfma_f32_16x16x32_bf16 v[100:103], v[154:157], v[214:217], v[100:103]
	v_mfma_f32_16x16x32_bf16 v[96:99], v[170:173], v[214:217], v[96:99]
	v_mfma_f32_16x16x32_bf16 v[84:87], v[154:157], v[226:229], v[84:87]
	v_mfma_f32_16x16x32_bf16 v[76:79], v[170:173], v[226:229], v[76:79]
	s_setprio 0
	s_setprio 1
	v_mfma_f32_16x16x32_bf16 v[108:111], v[174:177], v[190:193], 0
	v_mfma_f32_16x16x32_bf16 v[104:107], v[182:185], v[190:193], 0
	v_mfma_f32_16x16x32_bf16 v[92:95], v[174:177], v[194:197], 0
	v_mfma_f32_16x16x32_bf16 v[88:91], v[182:185], v[194:197], 0
	v_mfma_f32_16x16x32_bf16 v[80:83], v[174:177], v[206:209], 0
	v_mfma_f32_16x16x32_bf16 v[72:75], v[182:185], v[206:209], 0
	v_mfma_f32_16x16x32_bf16 v[68:71], v[174:177], v[210:213], 0
	v_mfma_f32_16x16x32_bf16 v[64:67], v[182:185], v[210:213], 0
	v_mfma_f32_16x16x32_bf16 v[108:111], v[178:181], v[198:201], v[108:111]
	v_mfma_f32_16x16x32_bf16 v[104:107], v[186:189], v[198:201], v[104:107]
	v_mfma_f32_16x16x32_bf16 v[92:95], v[178:181], v[202:205], v[92:95]
	v_mfma_f32_16x16x32_bf16 v[88:91], v[186:189], v[202:205], v[88:91]
	v_mfma_f32_16x16x32_bf16 v[80:83], v[178:181], v[214:217], v[80:83]
	v_mfma_f32_16x16x32_bf16 v[72:75], v[186:189], v[214:217], v[72:75]
	v_mfma_f32_16x16x32_bf16 v[68:71], v[178:181], v[226:229], v[68:71]
	v_mfma_f32_16x16x32_bf16 v[64:67], v[186:189], v[226:229], v[64:67]
	s_setprio 0
	s_barrier
	s_add_i32 s65, s65, s36
	v_lshl_add_u64 v[158:159], s[20:21], 0, v[132:133]
	s_mov_b32 m0, s65
	ds_read_b128 v[190:193], v145 offset:16384
	ds_read_b128 v[194:197], v145 offset:18432
	ds_read_b128 v[198:201], v146 offset:16384
	ds_read_b128 v[202:205], v146 offset:18432
	ds_read_b128 v[206:209], v145 offset:20480
	ds_read_b128 v[210:213], v145 offset:22528
	ds_read_b128 v[214:217], v146 offset:20480
	ds_read_b128 v[226:229], v146 offset:22528
	global_load_lds_dwordx4 v[158:159], off
	s_add_i32 m0, s65, 0x2000
	s_add_u32 s76, s20, 0x8000
	v_lshl_add_u64 v[218:219], s[20:21], 0, v[128:129]
	s_addc_u32 s77, s21, 0
	s_add_i32 s65, s73, s36
	global_load_lds_dwordx4 v[218:219], off
	v_lshl_add_u64 v[230:231], s[76:77], 0, v[132:133]
	s_mov_b32 m0, s65
	v_lshl_add_u64 v[232:233], s[30:31], 0, v[130:131]
	global_load_lds_dwordx4 v[230:231], off
	v_lshl_add_u64 v[230:231], s[76:77], 0, v[128:129]
	s_add_i32 m0, s65, 0x2000
	s_nop 0
	global_load_lds_dwordx4 v[230:231], off
	v_lshl_add_u64 v[230:231], s[30:31], 0, v[134:135]
	s_mov_b32 m0, s37
	s_nop 0
	global_load_lds_dwordx4 v[230:231], off
	s_mov_b32 m0, s41
	s_nop 0
	global_load_lds_dwordx4 v[232:233], off
	s_waitcnt vmcnt(8)
	s_waitcnt lgkmcnt(0)
	s_barrier
	s_setprio 1
	s_waitcnt lgkmcnt(0)
	v_mfma_f32_16x16x32_bf16 v[60:63], v[150:153], v[190:193], 0
	v_mfma_f32_16x16x32_bf16 v[56:59], v[166:169], v[190:193], 0
	v_mfma_f32_16x16x32_bf16 v[52:55], v[150:153], v[194:197], 0
	v_mfma_f32_16x16x32_bf16 v[44:47], v[166:169], v[194:197], 0
	v_mfma_f32_16x16x32_bf16 v[36:39], v[150:153], v[206:209], 0
	v_mfma_f32_16x16x32_bf16 v[28:31], v[166:169], v[206:209], 0
	v_mfma_f32_16x16x32_bf16 v[20:23], v[150:153], v[210:213], 0
	v_mfma_f32_16x16x32_bf16 v[12:15], v[166:169], v[210:213], 0
	v_mfma_f32_16x16x32_bf16 v[60:63], v[154:157], v[198:201], v[60:63]
	v_mfma_f32_16x16x32_bf16 v[56:59], v[170:173], v[198:201], v[56:59]
	v_mfma_f32_16x16x32_bf16 v[52:55], v[154:157], v[202:205], v[52:55]
	v_mfma_f32_16x16x32_bf16 v[44:47], v[170:173], v[202:205], v[44:47]
	v_mfma_f32_16x16x32_bf16 v[36:39], v[154:157], v[214:217], v[36:39]
	v_mfma_f32_16x16x32_bf16 v[28:31], v[170:173], v[214:217], v[28:31]
	v_mfma_f32_16x16x32_bf16 v[20:23], v[154:157], v[226:229], v[20:23]
	v_mfma_f32_16x16x32_bf16 v[12:15], v[170:173], v[226:229], v[12:15]
	s_setprio 0
	s_setprio 1
	v_mfma_f32_16x16x32_bf16 v[48:51], v[174:177], v[190:193], 0
	v_mfma_f32_16x16x32_bf16 v[40:43], v[182:185], v[190:193], 0
	v_mfma_f32_16x16x32_bf16 v[32:35], v[174:177], v[194:197], 0
	v_mfma_f32_16x16x32_bf16 v[24:27], v[182:185], v[194:197], 0
	v_mfma_f32_16x16x32_bf16 v[16:19], v[174:177], v[206:209], 0
	v_mfma_f32_16x16x32_bf16 v[8:11], v[182:185], v[206:209], 0
	v_mfma_f32_16x16x32_bf16 v[4:7], v[174:177], v[210:213], 0
	v_mfma_f32_16x16x32_bf16 v[0:3], v[182:185], v[210:213], 0
	v_mfma_f32_16x16x32_bf16 v[48:51], v[178:181], v[198:201], v[48:51]
	v_mfma_f32_16x16x32_bf16 v[40:43], v[186:189], v[198:201], v[40:43]
	v_mfma_f32_16x16x32_bf16 v[32:35], v[178:181], v[202:205], v[32:35]
	v_mfma_f32_16x16x32_bf16 v[24:27], v[186:189], v[202:205], v[24:27]
	v_mfma_f32_16x16x32_bf16 v[16:19], v[178:181], v[214:217], v[16:19]
	v_mfma_f32_16x16x32_bf16 v[8:11], v[186:189], v[214:217], v[8:11]
	v_mfma_f32_16x16x32_bf16 v[4:7], v[178:181], v[226:229], v[4:7]
	v_mfma_f32_16x16x32_bf16 v[0:3], v[186:189], v[226:229], v[0:3]
	s_setprio 0
	s_barrier
	s_add_i32 s65, 0, 0x18000
	v_add_u32_e32 v149, s65, v140
	v_add_u32_e32 v154, s65, v144
	ds_read_b128 v[150:153], v149
	ds_read_b128 v[154:157], v154
	v_add_u32_e32 v149, s87, v140
	s_add_i32 s73, 0, 0x1c000
	v_add_u32_e32 v162, s87, v144
	ds_read_b128 v[166:169], v149
	ds_read_b128 v[170:173], v162
	v_add_u32_e32 v149, s73, v140
	v_add_u32_e32 v162, s73, v144
	ds_read_b128 v[174:177], v149
	ds_read_b128 v[178:181], v162
	v_add_u32_e32 v149, s2, v140
	v_add_u32_e32 v162, s2, v144
	ds_read_b128 v[182:185], v149
	ds_read_b128 v[186:189], v162
	s_add_u32 s30, s30, 0x200000
	s_addc_u32 s31, s31, 0
	s_mov_b32 m0, s43
	v_lshl_add_u64 v[234:235], s[30:31], 0, v[134:135]
	ds_read_b128 v[190:193], v145 offset:32768
	ds_read_b128 v[194:197], v145 offset:34816
	ds_read_b128 v[198:201], v146 offset:32768
	ds_read_b128 v[202:205], v146 offset:34816
	ds_read_b128 v[206:209], v145 offset:36864
	ds_read_b128 v[210:213], v145 offset:38912
	ds_read_b128 v[214:217], v146 offset:36864
	ds_read_b128 v[226:229], v146 offset:38912
	global_load_lds_dwordx4 v[234:235], off
	v_lshl_add_u64 v[234:235], s[30:31], 0, v[130:131]
	s_mov_b32 m0, s46
	s_nop 0
	global_load_lds_dwordx4 v[234:235], off
	s_waitcnt vmcnt(8)
	s_waitcnt lgkmcnt(0)
	s_barrier
	s_setprio 1
	s_waitcnt lgkmcnt(0)
	v_mfma_f32_16x16x32_bf16 v[124:127], v[150:153], v[190:193], v[124:127]
	v_mfma_f32_16x16x32_bf16 v[120:123], v[166:169], v[190:193], v[120:123]
	v_mfma_f32_16x16x32_bf16 v[116:119], v[150:153], v[194:197], v[116:119]
	v_mfma_f32_16x16x32_bf16 v[112:115], v[166:169], v[194:197], v[112:115]
	v_mfma_f32_16x16x32_bf16 v[100:103], v[150:153], v[206:209], v[100:103]
	v_mfma_f32_16x16x32_bf16 v[96:99], v[166:169], v[206:209], v[96:99]
	v_mfma_f32_16x16x32_bf16 v[84:87], v[150:153], v[210:213], v[84:87]
	v_mfma_f32_16x16x32_bf16 v[76:79], v[166:169], v[210:213], v[76:79]
	v_mfma_f32_16x16x32_bf16 v[124:127], v[154:157], v[198:201], v[124:127]
	v_mfma_f32_16x16x32_bf16 v[120:123], v[170:173], v[198:201], v[120:123]
	v_mfma_f32_16x16x32_bf16 v[116:119], v[154:157], v[202:205], v[116:119]
	v_mfma_f32_16x16x32_bf16 v[112:115], v[170:173], v[202:205], v[112:115]
	v_mfma_f32_16x16x32_bf16 v[100:103], v[154:157], v[214:217], v[100:103]
	v_mfma_f32_16x16x32_bf16 v[96:99], v[170:173], v[214:217], v[96:99]
	v_mfma_f32_16x16x32_bf16 v[84:87], v[154:157], v[226:229], v[84:87]
	v_mfma_f32_16x16x32_bf16 v[76:79], v[170:173], v[226:229], v[76:79]
	s_setprio 0
	s_setprio 1
	v_mfma_f32_16x16x32_bf16 v[108:111], v[174:177], v[190:193], v[108:111]
	v_mfma_f32_16x16x32_bf16 v[104:107], v[182:185], v[190:193], v[104:107]
	v_mfma_f32_16x16x32_bf16 v[92:95], v[174:177], v[194:197], v[92:95]
	v_mfma_f32_16x16x32_bf16 v[88:91], v[182:185], v[194:197], v[88:91]
	v_mfma_f32_16x16x32_bf16 v[80:83], v[174:177], v[206:209], v[80:83]
	v_mfma_f32_16x16x32_bf16 v[72:75], v[182:185], v[206:209], v[72:75]
	v_mfma_f32_16x16x32_bf16 v[68:71], v[174:177], v[210:213], v[68:71]
	v_mfma_f32_16x16x32_bf16 v[64:67], v[182:185], v[210:213], v[64:67]
	v_mfma_f32_16x16x32_bf16 v[108:111], v[178:181], v[198:201], v[108:111]
	v_mfma_f32_16x16x32_bf16 v[104:107], v[186:189], v[198:201], v[104:107]
	v_mfma_f32_16x16x32_bf16 v[92:95], v[178:181], v[202:205], v[92:95]
	v_mfma_f32_16x16x32_bf16 v[88:91], v[186:189], v[202:205], v[88:91]
	v_mfma_f32_16x16x32_bf16 v[80:83], v[178:181], v[214:217], v[80:83]
	v_mfma_f32_16x16x32_bf16 v[72:75], v[186:189], v[214:217], v[72:75]
	v_mfma_f32_16x16x32_bf16 v[68:71], v[178:181], v[226:229], v[68:71]
	v_mfma_f32_16x16x32_bf16 v[64:67], v[186:189], v[226:229], v[64:67]
	s_setprio 0
	s_barrier
	s_add_i32 s30, s65, s36
	v_lshl_add_u64 v[158:159], v[158:159], 0, s[54:55]
	s_mov_b32 m0, s30
	ds_read_b128 v[190:193], v145 offset:49152
	ds_read_b128 v[194:197], v145 offset:51200
	ds_read_b128 v[198:201], v146 offset:49152
	ds_read_b128 v[202:205], v146 offset:51200
	ds_read_b128 v[206:209], v145 offset:53248
	ds_read_b128 v[210:213], v145 offset:55296
	ds_read_b128 v[214:217], v146 offset:53248
	ds_read_b128 v[226:229], v146 offset:55296
	global_load_lds_dwordx4 v[158:159], off
	s_add_i32 m0, s30, 0x2000
	s_add_u32 s20, s20, 0x8080
	v_lshl_add_u64 v[158:159], v[218:219], 0, s[54:55]
	s_addc_u32 s21, s21, 0
	s_add_i32 s30, s73, s36
	global_load_lds_dwordx4 v[158:159], off
	v_lshl_add_u64 v[158:159], s[20:21], 0, v[132:133]
	s_mov_b32 m0, s30
	s_nop 0
	global_load_lds_dwordx4 v[158:159], off
	v_lshl_add_u64 v[158:159], s[20:21], 0, v[128:129]
	s_add_i32 m0, s30, 0x2000
	s_nop 0
	global_load_lds_dwordx4 v[158:159], off
	v_lshl_add_u64 v[158:159], v[230:231], 0, s[54:55]
	s_mov_b32 m0, s47
	s_nop 0
	global_load_lds_dwordx4 v[158:159], off
	v_lshl_add_u64 v[158:159], v[232:233], 0, s[54:55]
	s_mov_b32 m0, s56
	s_nop 0
	global_load_lds_dwordx4 v[158:159], off
	s_waitcnt vmcnt(8)
	s_waitcnt lgkmcnt(0)
	s_barrier
	s_setprio 1
	s_waitcnt lgkmcnt(0)
	v_mfma_f32_16x16x32_bf16 v[60:63], v[150:153], v[190:193], v[60:63]
	v_mfma_f32_16x16x32_bf16 v[56:59], v[166:169], v[190:193], v[56:59]
	v_mfma_f32_16x16x32_bf16 v[52:55], v[150:153], v[194:197], v[52:55]
	v_mfma_f32_16x16x32_bf16 v[44:47], v[166:169], v[194:197], v[44:47]
	v_mfma_f32_16x16x32_bf16 v[36:39], v[150:153], v[206:209], v[36:39]
	v_mfma_f32_16x16x32_bf16 v[28:31], v[166:169], v[206:209], v[28:31]
	v_mfma_f32_16x16x32_bf16 v[20:23], v[150:153], v[210:213], v[20:23]
	v_mfma_f32_16x16x32_bf16 v[12:15], v[166:169], v[210:213], v[12:15]
	v_mfma_f32_16x16x32_bf16 v[60:63], v[154:157], v[198:201], v[60:63]
	v_mfma_f32_16x16x32_bf16 v[56:59], v[170:173], v[198:201], v[56:59]
	v_mfma_f32_16x16x32_bf16 v[52:55], v[154:157], v[202:205], v[52:55]
	v_mfma_f32_16x16x32_bf16 v[44:47], v[170:173], v[202:205], v[44:47]
	v_mfma_f32_16x16x32_bf16 v[36:39], v[154:157], v[214:217], v[36:39]
	v_mfma_f32_16x16x32_bf16 v[28:31], v[170:173], v[214:217], v[28:31]
	v_mfma_f32_16x16x32_bf16 v[20:23], v[154:157], v[226:229], v[20:23]
	v_mfma_f32_16x16x32_bf16 v[12:15], v[170:173], v[226:229], v[12:15]
	s_setprio 0
	s_setprio 1
	v_mfma_f32_16x16x32_bf16 v[48:51], v[174:177], v[190:193], v[48:51]
	v_mfma_f32_16x16x32_bf16 v[40:43], v[182:185], v[190:193], v[40:43]
	v_mfma_f32_16x16x32_bf16 v[32:35], v[174:177], v[194:197], v[32:35]
	v_mfma_f32_16x16x32_bf16 v[24:27], v[182:185], v[194:197], v[24:27]
	v_mfma_f32_16x16x32_bf16 v[16:19], v[174:177], v[206:209], v[16:19]
	v_mfma_f32_16x16x32_bf16 v[8:11], v[182:185], v[206:209], v[8:11]
	v_mfma_f32_16x16x32_bf16 v[4:7], v[174:177], v[210:213], v[4:7]
	v_mfma_f32_16x16x32_bf16 v[0:3], v[182:185], v[210:213], v[0:3]
	v_mfma_f32_16x16x32_bf16 v[48:51], v[178:181], v[198:201], v[48:51]
	v_mfma_f32_16x16x32_bf16 v[40:43], v[186:189], v[198:201], v[40:43]
	v_mfma_f32_16x16x32_bf16 v[32:35], v[178:181], v[202:205], v[32:35]
	v_mfma_f32_16x16x32_bf16 v[24:27], v[186:189], v[202:205], v[24:27]
	v_mfma_f32_16x16x32_bf16 v[16:19], v[178:181], v[214:217], v[16:19]
	v_mfma_f32_16x16x32_bf16 v[8:11], v[186:189], v[214:217], v[8:11]
	v_mfma_f32_16x16x32_bf16 v[4:7], v[178:181], v[226:229], v[4:7]
	v_mfma_f32_16x16x32_bf16 v[0:3], v[186:189], v[226:229], v[0:3]
	s_setprio 0
	s_barrier
	s_add_i32 s72, s72, 2
	s_add_u32 s18, s18, 0x100
	s_addc_u32 s19, s19, 0
	s_add_u32 s70, s70, 0x100
	s_addc_u32 s71, s71, 0
	s_cmp_gt_u32 s72, 5
	s_cbranch_scc1 .Lepi_856

.LBB0_906:
	s_ashr_i32 s13, s12, 31
	s_lshl_b64 s[14:15], s[12:13], 21
	s_add_u32 s14, s52, s14
	s_addc_u32 s15, s53, s15
	s_and_b64 s[16:17], s[6:7], exec
	s_cselect_b32 s13, s15, s19
	s_cselect_b32 s69, s14, s18
	s_ashr_i32 s11, s10, 31
	s_lshl_b64 s[16:17], s[10:11], 21
	s_add_u32 s16, s34, s16
	s_addc_u32 s17, s35, s17
	s_and_b64 s[30:31], s[6:7], exec
	s_cselect_b32 s11, s17, s21
	s_cselect_b32 s70, s16, s20
	s_add_u32 s18, s18, 0x100080
	s_addc_u32 s19, s19, 0
	s_add_u32 s71, s20, 0x100
	s_addc_u32 s72, s21, 0
	s_mov_b32 s73, -2
	s_add_u32 s20, s18, 0xfff00080
	s_addc_u32 s21, s19, -1
	s_add_i32 s65, 0, 0x10000
	s_cmp_eq_u32 s73, 60
	v_add_u32_e32 v149, s65, v140
	v_add_u32_e32 v154, s65, v144
	s_cselect_b32 s31, s13, s21
	s_cselect_b32 s30, s69, s20
	ds_read_b128 v[150:153], v149
	ds_read_b128 v[154:157], v154
	v_add_u32_e32 v149, s1, v140
	s_cselect_b32 s21, s11, s72
	s_cselect_b32 s20, s70, s71
	s_add_i32 s84, 0, 0x14000
	v_add_u32_e32 v158, s1, v144
	ds_read_b128 v[166:169], v149
	ds_read_b128 v[170:173], v158
	v_add_u32_e32 v149, s84, v140
	v_add_u32_e32 v158, s84, v144
	ds_read_b128 v[174:177], v149
	ds_read_b128 v[178:181], v158
	v_add_u32_e32 v149, s86, v140
	v_add_u32_e32 v158, s86, v144
	ds_read_b128 v[182:185], v149
	ds_read_b128 v[186:189], v158
	v_lshl_add_u64 v[158:159], s[18:19], 0, v[136:137]
	s_add_i32 m0, s37, 0xc000
	ds_read_b128 v[190:193], v145
	ds_read_b128 v[194:197], v145 offset:2048
	ds_read_b128 v[198:201], v146
	ds_read_b128 v[202:205], v146 offset:2048
	ds_read_b128 v[206:209], v145 offset:4096
	ds_read_b128 v[210:213], v145 offset:6144
	ds_read_b128 v[214:217], v146 offset:4096
	ds_read_b128 v[226:229], v146 offset:6144
	global_load_lds_dwordx4 v[158:159], off
	v_lshl_add_u64 v[158:159], s[18:19], 0, v[138:139]
	s_add_i32 m0, s37, 0xe000
	s_nop 0
	global_load_lds_dwordx4 v[158:159], off
	s_waitcnt vmcnt(8)
	s_waitcnt lgkmcnt(0)
	s_barrier
	s_setprio 1
	s_waitcnt lgkmcnt(0)
	v_mfma_f32_16x16x32_bf16 v[124:127], v[150:153], v[190:193], 0
	v_mfma_f32_16x16x32_bf16 v[120:123], v[166:169], v[190:193], 0
	v_mfma_f32_16x16x32_bf16 v[116:119], v[150:153], v[194:197], 0
	v_mfma_f32_16x16x32_bf16 v[112:115], v[166:169], v[194:197], 0
	v_mfma_f32_16x16x32_bf16 v[100:103], v[150:153], v[206:209], 0
	v_mfma_f32_16x16x32_bf16 v[96:99], v[166:169], v[206:209], 0
	v_mfma_f32_16x16x32_bf16 v[84:87], v[150:153], v[210:213], 0
	v_mfma_f32_16x16x32_bf16 v[76:79], v[166:169], v[210:213], 0
	v_mfma_f32_16x16x32_bf16 v[124:127], v[154:157], v[198:201], v[124:127]
	v_mfma_f32_16x16x32_bf16 v[120:123], v[170:173], v[198:201], v[120:123]
	v_mfma_f32_16x16x32_bf16 v[116:119], v[154:157], v[202:205], v[116:119]
	v_mfma_f32_16x16x32_bf16 v[112:115], v[170:173], v[202:205], v[112:115]
	v_mfma_f32_16x16x32_bf16 v[100:103], v[154:157], v[214:217], v[100:103]
	v_mfma_f32_16x16x32_bf16 v[96:99], v[170:173], v[214:217], v[96:99]
	v_mfma_f32_16x16x32_bf16 v[84:87], v[154:157], v[226:229], v[84:87]
	v_mfma_f32_16x16x32_bf16 v[76:79], v[170:173], v[226:229], v[76:79]
	s_setprio 0
	s_setprio 1
	v_mfma_f32_16x16x32_bf16 v[108:111], v[174:177], v[190:193], 0
	v_mfma_f32_16x16x32_bf16 v[104:107], v[182:185], v[190:193], 0
	v_mfma_f32_16x16x32_bf16 v[92:95], v[174:177], v[194:197], 0
	v_mfma_f32_16x16x32_bf16 v[88:91], v[182:185], v[194:197], 0
	v_mfma_f32_16x16x32_bf16 v[80:83], v[174:177], v[206:209], 0
	v_mfma_f32_16x16x32_bf16 v[72:75], v[182:185], v[206:209], 0
	v_mfma_f32_16x16x32_bf16 v[68:71], v[174:177], v[210:213], 0
	v_mfma_f32_16x16x32_bf16 v[64:67], v[182:185], v[210:213], 0
	v_mfma_f32_16x16x32_bf16 v[108:111], v[178:181], v[198:201], v[108:111]
	v_mfma_f32_16x16x32_bf16 v[104:107], v[186:189], v[198:201], v[104:107]
	v_mfma_f32_16x16x32_bf16 v[92:95], v[178:181], v[202:205], v[92:95]
	v_mfma_f32_16x16x32_bf16 v[88:91], v[186:189], v[202:205], v[88:91]
	v_mfma_f32_16x16x32_bf16 v[80:83], v[178:181], v[214:217], v[80:83]
	v_mfma_f32_16x16x32_bf16 v[72:75], v[186:189], v[214:217], v[72:75]
	v_mfma_f32_16x16x32_bf16 v[68:71], v[178:181], v[226:229], v[68:71]
	v_mfma_f32_16x16x32_bf16 v[64:67], v[186:189], v[226:229], v[64:67]
	s_setprio 0
	s_barrier
	s_add_i32 s65, s65, s36
	v_lshl_add_u64 v[158:159], s[20:21], 0, v[132:133]
	s_mov_b32 m0, s65
	ds_read_b128 v[190:193], v145 offset:16384
	ds_read_b128 v[194:197], v145 offset:18432
	ds_read_b128 v[198:201], v146 offset:16384
	ds_read_b128 v[202:205], v146 offset:18432
	ds_read_b128 v[206:209], v145 offset:20480
	ds_read_b128 v[210:213], v145 offset:22528
	ds_read_b128 v[214:217], v146 offset:20480
	ds_read_b128 v[226:229], v146 offset:22528
	global_load_lds_dwordx4 v[158:159], off
	s_add_i32 m0, s65, 0x2000
	s_add_u32 s76, s20, 0x40000
	v_lshl_add_u64 v[218:219], s[20:21], 0, v[128:129]
	s_addc_u32 s77, s21, 0
	s_add_i32 s65, s84, s36
	global_load_lds_dwordx4 v[218:219], off
	v_lshl_add_u64 v[230:231], s[76:77], 0, v[132:133]
	s_mov_b32 m0, s65
	v_lshl_add_u64 v[232:233], s[30:31], 0, v[130:131]
	global_load_lds_dwordx4 v[230:231], off
	v_lshl_add_u64 v[230:231], s[76:77], 0, v[128:129]
	s_add_i32 m0, s65, 0x2000
	s_nop 0
	global_load_lds_dwordx4 v[230:231], off
	v_lshl_add_u64 v[230:231], s[30:31], 0, v[134:135]
	s_mov_b32 m0, s37
	s_nop 0
	global_load_lds_dwordx4 v[230:231], off
	s_mov_b32 m0, s41
	s_nop 0
	global_load_lds_dwordx4 v[232:233], off
	s_waitcnt vmcnt(8)
	s_waitcnt lgkmcnt(0)
	s_barrier
	s_setprio 1
	s_waitcnt lgkmcnt(0)
	v_mfma_f32_16x16x32_bf16 v[60:63], v[150:153], v[190:193], 0
	v_mfma_f32_16x16x32_bf16 v[56:59], v[166:169], v[190:193], 0
	v_mfma_f32_16x16x32_bf16 v[52:55], v[150:153], v[194:197], 0
	v_mfma_f32_16x16x32_bf16 v[44:47], v[166:169], v[194:197], 0
	v_mfma_f32_16x16x32_bf16 v[36:39], v[150:153], v[206:209], 0
	v_mfma_f32_16x16x32_bf16 v[28:31], v[166:169], v[206:209], 0
	v_mfma_f32_16x16x32_bf16 v[20:23], v[150:153], v[210:213], 0
	v_mfma_f32_16x16x32_bf16 v[12:15], v[166:169], v[210:213], 0
	v_mfma_f32_16x16x32_bf16 v[60:63], v[154:157], v[198:201], v[60:63]
	v_mfma_f32_16x16x32_bf16 v[56:59], v[170:173], v[198:201], v[56:59]
	v_mfma_f32_16x16x32_bf16 v[52:55], v[154:157], v[202:205], v[52:55]
	v_mfma_f32_16x16x32_bf16 v[44:47], v[170:173], v[202:205], v[44:47]
	v_mfma_f32_16x16x32_bf16 v[36:39], v[154:157], v[214:217], v[36:39]
	v_mfma_f32_16x16x32_bf16 v[28:31], v[170:173], v[214:217], v[28:31]
	v_mfma_f32_16x16x32_bf16 v[20:23], v[154:157], v[226:229], v[20:23]
	v_mfma_f32_16x16x32_bf16 v[12:15], v[170:173], v[226:229], v[12:15]
	s_setprio 0
	s_setprio 1
	v_mfma_f32_16x16x32_bf16 v[48:51], v[174:177], v[190:193], 0
	v_mfma_f32_16x16x32_bf16 v[40:43], v[182:185], v[190:193], 0
	v_mfma_f32_16x16x32_bf16 v[32:35], v[174:177], v[194:197], 0
	v_mfma_f32_16x16x32_bf16 v[24:27], v[182:185], v[194:197], 0
	v_mfma_f32_16x16x32_bf16 v[16:19], v[174:177], v[206:209], 0
	v_mfma_f32_16x16x32_bf16 v[8:11], v[182:185], v[206:209], 0
	v_mfma_f32_16x16x32_bf16 v[4:7], v[174:177], v[210:213], 0
	v_mfma_f32_16x16x32_bf16 v[0:3], v[182:185], v[210:213], 0
	v_mfma_f32_16x16x32_bf16 v[48:51], v[178:181], v[198:201], v[48:51]
	v_mfma_f32_16x16x32_bf16 v[40:43], v[186:189], v[198:201], v[40:43]
	v_mfma_f32_16x16x32_bf16 v[32:35], v[178:181], v[202:205], v[32:35]
	v_mfma_f32_16x16x32_bf16 v[24:27], v[186:189], v[202:205], v[24:27]
	v_mfma_f32_16x16x32_bf16 v[16:19], v[178:181], v[214:217], v[16:19]
	v_mfma_f32_16x16x32_bf16 v[8:11], v[186:189], v[214:217], v[8:11]
	v_mfma_f32_16x16x32_bf16 v[4:7], v[178:181], v[226:229], v[4:7]
	v_mfma_f32_16x16x32_bf16 v[0:3], v[186:189], v[226:229], v[0:3]
	s_setprio 0
	s_barrier
	s_add_i32 s65, 0, 0x18000
	v_add_u32_e32 v149, s65, v140
	v_add_u32_e32 v154, s65, v144
	ds_read_b128 v[150:153], v149
	ds_read_b128 v[154:157], v154
	v_add_u32_e32 v149, s87, v140
	s_add_i32 s76, 0, 0x1c000
	v_add_u32_e32 v162, s87, v144
	ds_read_b128 v[166:169], v149
	ds_read_b128 v[170:173], v162
	v_add_u32_e32 v149, s76, v140
	v_add_u32_e32 v162, s76, v144
	ds_read_b128 v[174:177], v149
	ds_read_b128 v[178:181], v162
	v_add_u32_e32 v149, s2, v140
	v_add_u32_e32 v162, s2, v144
	ds_read_b128 v[182:185], v149
	ds_read_b128 v[186:189], v162
	s_add_u32 s30, s30, 0x100000
	s_addc_u32 s31, s31, 0
	s_mov_b32 m0, s43
	v_lshl_add_u64 v[234:235], s[30:31], 0, v[134:135]
	ds_read_b128 v[190:193], v145 offset:32768
	ds_read_b128 v[194:197], v145 offset:34816
	ds_read_b128 v[198:201], v146 offset:32768
	ds_read_b128 v[202:205], v146 offset:34816
	ds_read_b128 v[206:209], v145 offset:36864
	ds_read_b128 v[210:213], v145 offset:38912
	ds_read_b128 v[214:217], v146 offset:36864
	ds_read_b128 v[226:229], v146 offset:38912
	global_load_lds_dwordx4 v[234:235], off
	v_lshl_add_u64 v[234:235], s[30:31], 0, v[130:131]
	s_mov_b32 m0, s46
	s_nop 0
	global_load_lds_dwordx4 v[234:235], off
	s_waitcnt vmcnt(8)
	s_waitcnt lgkmcnt(0)
	s_barrier
	s_setprio 1
	s_waitcnt lgkmcnt(0)
	v_mfma_f32_16x16x32_bf16 v[124:127], v[150:153], v[190:193], v[124:127]
	v_mfma_f32_16x16x32_bf16 v[120:123], v[166:169], v[190:193], v[120:123]
	v_mfma_f32_16x16x32_bf16 v[116:119], v[150:153], v[194:197], v[116:119]
	v_mfma_f32_16x16x32_bf16 v[112:115], v[166:169], v[194:197], v[112:115]
	v_mfma_f32_16x16x32_bf16 v[100:103], v[150:153], v[206:209], v[100:103]
	v_mfma_f32_16x16x32_bf16 v[96:99], v[166:169], v[206:209], v[96:99]
	v_mfma_f32_16x16x32_bf16 v[84:87], v[150:153], v[210:213], v[84:87]
	v_mfma_f32_16x16x32_bf16 v[76:79], v[166:169], v[210:213], v[76:79]
	v_mfma_f32_16x16x32_bf16 v[124:127], v[154:157], v[198:201], v[124:127]
	v_mfma_f32_16x16x32_bf16 v[120:123], v[170:173], v[198:201], v[120:123]
	v_mfma_f32_16x16x32_bf16 v[116:119], v[154:157], v[202:205], v[116:119]
	v_mfma_f32_16x16x32_bf16 v[112:115], v[170:173], v[202:205], v[112:115]
	v_mfma_f32_16x16x32_bf16 v[100:103], v[154:157], v[214:217], v[100:103]
	v_mfma_f32_16x16x32_bf16 v[96:99], v[170:173], v[214:217], v[96:99]
	v_mfma_f32_16x16x32_bf16 v[84:87], v[154:157], v[226:229], v[84:87]
	v_mfma_f32_16x16x32_bf16 v[76:79], v[170:173], v[226:229], v[76:79]
	s_setprio 0
	s_setprio 1
	v_mfma_f32_16x16x32_bf16 v[108:111], v[174:177], v[190:193], v[108:111]
	v_mfma_f32_16x16x32_bf16 v[104:107], v[182:185], v[190:193], v[104:107]
	v_mfma_f32_16x16x32_bf16 v[92:95], v[174:177], v[194:197], v[92:95]
	v_mfma_f32_16x16x32_bf16 v[88:91], v[182:185], v[194:197], v[88:91]
	v_mfma_f32_16x16x32_bf16 v[80:83], v[174:177], v[206:209], v[80:83]
	v_mfma_f32_16x16x32_bf16 v[72:75], v[182:185], v[206:209], v[72:75]
	v_mfma_f32_16x16x32_bf16 v[68:71], v[174:177], v[210:213], v[68:71]
	v_mfma_f32_16x16x32_bf16 v[64:67], v[182:185], v[210:213], v[64:67]
	v_mfma_f32_16x16x32_bf16 v[108:111], v[178:181], v[198:201], v[108:111]
	v_mfma_f32_16x16x32_bf16 v[104:107], v[186:189], v[198:201], v[104:107]
	v_mfma_f32_16x16x32_bf16 v[92:95], v[178:181], v[202:205], v[92:95]
	v_mfma_f32_16x16x32_bf16 v[88:91], v[186:189], v[202:205], v[88:91]
	v_mfma_f32_16x16x32_bf16 v[80:83], v[178:181], v[214:217], v[80:83]
	v_mfma_f32_16x16x32_bf16 v[72:75], v[186:189], v[214:217], v[72:75]
	v_mfma_f32_16x16x32_bf16 v[68:71], v[178:181], v[226:229], v[68:71]
	v_mfma_f32_16x16x32_bf16 v[64:67], v[186:189], v[226:229], v[64:67]
	s_setprio 0
	s_barrier
	s_add_i32 s30, s65, s36
	v_lshl_add_u64 v[158:159], v[158:159], 0, s[54:55]
	s_mov_b32 m0, s30
	ds_read_b128 v[190:193], v145 offset:49152
	ds_read_b128 v[194:197], v145 offset:51200
	ds_read_b128 v[198:201], v146 offset:49152
	ds_read_b128 v[202:205], v146 offset:51200
	ds_read_b128 v[206:209], v145 offset:53248
	ds_read_b128 v[210:213], v145 offset:55296
	ds_read_b128 v[214:217], v146 offset:53248
	ds_read_b128 v[226:229], v146 offset:55296
	global_load_lds_dwordx4 v[158:159], off
	s_add_i32 m0, s30, 0x2000
	s_add_u32 s20, s20, 0x40080
	v_lshl_add_u64 v[158:159], v[218:219], 0, s[54:55]
	s_addc_u32 s21, s21, 0
	s_add_i32 s30, s76, s36
	global_load_lds_dwordx4 v[158:159], off
	v_lshl_add_u64 v[158:159], s[20:21], 0, v[132:133]
	s_mov_b32 m0, s30
	s_nop 0
	global_load_lds_dwordx4 v[158:159], off
	v_lshl_add_u64 v[158:159], s[20:21], 0, v[128:129]
	s_add_i32 m0, s30, 0x2000
	s_nop 0
	global_load_lds_dwordx4 v[158:159], off
	v_lshl_add_u64 v[158:159], v[230:231], 0, s[54:55]
	s_mov_b32 m0, s47
	s_nop 0
	global_load_lds_dwordx4 v[158:159], off
	v_lshl_add_u64 v[158:159], v[232:233], 0, s[54:55]
	s_mov_b32 m0, s56
	s_nop 0
	global_load_lds_dwordx4 v[158:159], off
	s_waitcnt vmcnt(8)
	s_waitcnt lgkmcnt(0)
	s_barrier
	s_setprio 1
	s_waitcnt lgkmcnt(0)
	v_mfma_f32_16x16x32_bf16 v[60:63], v[150:153], v[190:193], v[60:63]
	v_mfma_f32_16x16x32_bf16 v[56:59], v[166:169], v[190:193], v[56:59]
	v_mfma_f32_16x16x32_bf16 v[52:55], v[150:153], v[194:197], v[52:55]
	v_mfma_f32_16x16x32_bf16 v[44:47], v[166:169], v[194:197], v[44:47]
	v_mfma_f32_16x16x32_bf16 v[36:39], v[150:153], v[206:209], v[36:39]
	v_mfma_f32_16x16x32_bf16 v[28:31], v[166:169], v[206:209], v[28:31]
	v_mfma_f32_16x16x32_bf16 v[20:23], v[150:153], v[210:213], v[20:23]
	v_mfma_f32_16x16x32_bf16 v[12:15], v[166:169], v[210:213], v[12:15]
	v_mfma_f32_16x16x32_bf16 v[60:63], v[154:157], v[198:201], v[60:63]
	v_mfma_f32_16x16x32_bf16 v[56:59], v[170:173], v[198:201], v[56:59]
	v_mfma_f32_16x16x32_bf16 v[52:55], v[154:157], v[202:205], v[52:55]
	v_mfma_f32_16x16x32_bf16 v[44:47], v[170:173], v[202:205], v[44:47]
	v_mfma_f32_16x16x32_bf16 v[36:39], v[154:157], v[214:217], v[36:39]
	v_mfma_f32_16x16x32_bf16 v[28:31], v[170:173], v[214:217], v[28:31]
	v_mfma_f32_16x16x32_bf16 v[20:23], v[154:157], v[226:229], v[20:23]
	v_mfma_f32_16x16x32_bf16 v[12:15], v[170:173], v[226:229], v[12:15]
	s_setprio 0
	s_setprio 1
	v_mfma_f32_16x16x32_bf16 v[48:51], v[174:177], v[190:193], v[48:51]
	v_mfma_f32_16x16x32_bf16 v[40:43], v[182:185], v[190:193], v[40:43]
	v_mfma_f32_16x16x32_bf16 v[32:35], v[174:177], v[194:197], v[32:35]
	v_mfma_f32_16x16x32_bf16 v[24:27], v[182:185], v[194:197], v[24:27]
	v_mfma_f32_16x16x32_bf16 v[16:19], v[174:177], v[206:209], v[16:19]
	v_mfma_f32_16x16x32_bf16 v[8:11], v[182:185], v[206:209], v[8:11]
	v_mfma_f32_16x16x32_bf16 v[4:7], v[174:177], v[210:213], v[4:7]
	v_mfma_f32_16x16x32_bf16 v[0:3], v[182:185], v[210:213], v[0:3]
	v_mfma_f32_16x16x32_bf16 v[48:51], v[178:181], v[198:201], v[48:51]
	v_mfma_f32_16x16x32_bf16 v[40:43], v[186:189], v[198:201], v[40:43]
	v_mfma_f32_16x16x32_bf16 v[32:35], v[178:181], v[202:205], v[32:35]
	v_mfma_f32_16x16x32_bf16 v[24:27], v[186:189], v[202:205], v[24:27]
	v_mfma_f32_16x16x32_bf16 v[16:19], v[178:181], v[214:217], v[16:19]
	v_mfma_f32_16x16x32_bf16 v[8:11], v[186:189], v[214:217], v[8:11]
	v_mfma_f32_16x16x32_bf16 v[4:7], v[178:181], v[226:229], v[4:7]
	v_mfma_f32_16x16x32_bf16 v[0:3], v[186:189], v[226:229], v[0:3]
	s_setprio 0
	s_barrier
	s_add_i32 s73, s73, 2
	s_add_u32 s18, s18, 0x100
	s_addc_u32 s19, s19, 0
	s_add_u32 s71, s71, 0x100
	s_addc_u32 s72, s72, 0
	s_cmp_gt_u32 s73, 61
	s_cbranch_scc1 .Lepi_907

.LBB0_1039:
	s_ashr_i32 s17, s16, 31
	s_lshl_b64 s[18:19], s[16:17], 20
	s_add_u32 s18, s38, s18
	s_addc_u32 s19, s39, s19
	s_and_b64 s[20:21], s[6:7], exec
	s_cselect_b32 s17, s19, s31
	s_cselect_b32 s76, s18, s30
	s_ashr_i32 s11, s10, 31
	s_lshl_b64 s[20:21], s[10:11], 20
	s_add_u32 s20, s41, s20
	s_addc_u32 s21, s43, s21
	s_and_b64 s[36:37], s[6:7], exec
	s_cselect_b32 s11, s21, s35
	s_cselect_b32 s77, s20, s34
	s_add_u32 s30, s30, 0x80080
	s_addc_u32 s31, s31, 0
	s_add_u32 s84, s34, 0x100
	s_addc_u32 s88, s35, 0
	s_mov_b32 s89, -2
	s_add_u32 s34, s30, 0xfff80080
	s_addc_u32 s35, s31, -1
	s_add_i32 s65, 0, 0x10000
	s_cmp_eq_u32 s89, 28
	v_add_u32_e32 v140, s65, v142
	s_cselect_b32 s37, s17, s35
	s_cselect_b32 s36, s76, s34
	v_add_u32_e32 v141, s65, v146
	ds_read_b128 v[152:155], v140
	ds_read_b128 v[156:159], v141
	v_add_u32_e32 v140, s1, v142
	s_cselect_b32 s35, s11, s88
	s_cselect_b32 s34, s77, s84
	s_add_i32 s94, 0, 0x14000
	v_add_u32_e32 v141, s1, v146
	ds_read_b128 v[166:169], v140
	ds_read_b128 v[170:173], v141
	v_add_u32_e32 v140, s94, v142
	v_add_u32_e32 v141, s94, v146
	ds_read_b128 v[174:177], v140
	ds_read_b128 v[178:181], v141
	v_add_u32_e32 v140, s86, v142
	v_add_u32_e32 v141, s86, v146
	ds_read_b128 v[182:185], v140
	ds_read_b128 v[186:189], v141
	v_lshl_add_u64 v[140:141], s[30:31], 0, v[136:137]
	s_add_i32 m0, s47, 0xc000
	ds_read_b128 v[190:193], v147
	ds_read_b128 v[194:197], v147 offset:2048
	ds_read_b128 v[198:201], v148
	ds_read_b128 v[202:205], v148 offset:2048
	ds_read_b128 v[206:209], v147 offset:4096
	ds_read_b128 v[210:213], v147 offset:6144
	ds_read_b128 v[214:217], v148 offset:4096
	ds_read_b128 v[226:229], v148 offset:6144
	global_load_lds_dwordx4 v[140:141], off
	v_lshl_add_u64 v[140:141], s[30:31], 0, v[138:139]
	s_add_i32 m0, s47, 0xe000
	s_nop 0
	global_load_lds_dwordx4 v[140:141], off
	s_waitcnt vmcnt(8)
	s_waitcnt lgkmcnt(0)
	s_barrier
	s_setprio 1
	s_waitcnt lgkmcnt(0)
	v_mfma_f32_16x16x32_bf16 v[124:127], v[152:155], v[190:193], 0
	v_mfma_f32_16x16x32_bf16 v[120:123], v[166:169], v[190:193], 0
	v_mfma_f32_16x16x32_bf16 v[112:115], v[152:155], v[194:197], 0
	v_mfma_f32_16x16x32_bf16 v[104:107], v[166:169], v[194:197], 0
	v_mfma_f32_16x16x32_bf16 v[92:95], v[152:155], v[206:209], 0
	v_mfma_f32_16x16x32_bf16 v[88:91], v[166:169], v[206:209], 0
	v_mfma_f32_16x16x32_bf16 v[76:79], v[152:155], v[210:213], 0
	v_mfma_f32_16x16x32_bf16 v[72:75], v[166:169], v[210:213], 0
	v_mfma_f32_16x16x32_bf16 v[124:127], v[156:159], v[198:201], v[124:127]
	v_mfma_f32_16x16x32_bf16 v[120:123], v[170:173], v[198:201], v[120:123]
	v_mfma_f32_16x16x32_bf16 v[112:115], v[156:159], v[202:205], v[112:115]
	v_mfma_f32_16x16x32_bf16 v[104:107], v[170:173], v[202:205], v[104:107]
	v_mfma_f32_16x16x32_bf16 v[92:95], v[156:159], v[214:217], v[92:95]
	v_mfma_f32_16x16x32_bf16 v[88:91], v[170:173], v[214:217], v[88:91]
	v_mfma_f32_16x16x32_bf16 v[76:79], v[156:159], v[226:229], v[76:79]
	v_mfma_f32_16x16x32_bf16 v[72:75], v[170:173], v[226:229], v[72:75]
	s_setprio 0
	s_setprio 1
	v_mfma_f32_16x16x32_bf16 v[116:119], v[174:177], v[190:193], 0
	v_mfma_f32_16x16x32_bf16 v[108:111], v[182:185], v[190:193], 0
	v_mfma_f32_16x16x32_bf16 v[100:103], v[174:177], v[194:197], 0
	v_mfma_f32_16x16x32_bf16 v[96:99], v[182:185], v[194:197], 0
	v_mfma_f32_16x16x32_bf16 v[84:87], v[174:177], v[206:209], 0
	v_mfma_f32_16x16x32_bf16 v[80:83], v[182:185], v[206:209], 0
	v_mfma_f32_16x16x32_bf16 v[68:71], v[174:177], v[210:213], 0
	v_mfma_f32_16x16x32_bf16 v[64:67], v[182:185], v[210:213], 0
	v_mfma_f32_16x16x32_bf16 v[116:119], v[178:181], v[198:201], v[116:119]
	v_mfma_f32_16x16x32_bf16 v[108:111], v[186:189], v[198:201], v[108:111]
	v_mfma_f32_16x16x32_bf16 v[100:103], v[178:181], v[202:205], v[100:103]
	v_mfma_f32_16x16x32_bf16 v[96:99], v[186:189], v[202:205], v[96:99]
	v_mfma_f32_16x16x32_bf16 v[84:87], v[178:181], v[214:217], v[84:87]
	v_mfma_f32_16x16x32_bf16 v[80:83], v[186:189], v[214:217], v[80:83]
	v_mfma_f32_16x16x32_bf16 v[68:71], v[178:181], v[226:229], v[68:71]
	v_mfma_f32_16x16x32_bf16 v[64:67], v[186:189], v[226:229], v[64:67]
	s_setprio 0
	s_barrier
	s_add_i32 s65, s65, s46
	v_lshl_add_u64 v[140:141], s[34:35], 0, v[132:133]
	s_mov_b32 m0, s65
	ds_read_b128 v[190:193], v147 offset:16384
	ds_read_b128 v[194:197], v147 offset:18432
	ds_read_b128 v[198:201], v148 offset:16384
	ds_read_b128 v[202:205], v148 offset:18432
	ds_read_b128 v[206:209], v147 offset:20480
	ds_read_b128 v[210:213], v147 offset:22528
	ds_read_b128 v[214:217], v148 offset:20480
	ds_read_b128 v[226:229], v148 offset:22528
	global_load_lds_dwordx4 v[140:141], off
	s_add_i32 m0, s65, 0x2000
	s_add_u32 s90, s34, 0x20000
	v_lshl_add_u64 v[162:163], s[34:35], 0, v[128:129]
	s_addc_u32 s91, s35, 0
	s_add_i32 s65, s94, s46
	global_load_lds_dwordx4 v[162:163], off
	v_lshl_add_u64 v[218:219], s[90:91], 0, v[132:133]
	s_mov_b32 m0, s65
	v_lshl_add_u64 v[230:231], s[36:37], 0, v[130:131]
	global_load_lds_dwordx4 v[218:219], off
	v_lshl_add_u64 v[218:219], s[90:91], 0, v[128:129]
	s_add_i32 m0, s65, 0x2000
	s_nop 0
	global_load_lds_dwordx4 v[218:219], off
	v_lshl_add_u64 v[218:219], s[36:37], 0, v[134:135]
	s_mov_b32 m0, s47
	s_nop 0
	global_load_lds_dwordx4 v[218:219], off
	s_mov_b32 m0, s56
	s_nop 0
	global_load_lds_dwordx4 v[230:231], off
	s_waitcnt vmcnt(8)
	s_waitcnt lgkmcnt(0)
	s_barrier
	s_setprio 1
	s_waitcnt lgkmcnt(0)
	v_mfma_f32_16x16x32_bf16 v[60:63], v[152:155], v[190:193], 0
	v_mfma_f32_16x16x32_bf16 v[56:59], v[166:169], v[190:193], 0
	v_mfma_f32_16x16x32_bf16 v[44:47], v[152:155], v[194:197], 0
	v_mfma_f32_16x16x32_bf16 v[40:43], v[166:169], v[194:197], 0
	v_mfma_f32_16x16x32_bf16 v[28:31], v[152:155], v[206:209], 0
	v_mfma_f32_16x16x32_bf16 v[24:27], v[166:169], v[206:209], 0
	v_mfma_f32_16x16x32_bf16 v[12:15], v[152:155], v[210:213], 0
	v_mfma_f32_16x16x32_bf16 v[8:11], v[166:169], v[210:213], 0
	v_mfma_f32_16x16x32_bf16 v[60:63], v[156:159], v[198:201], v[60:63]
	v_mfma_f32_16x16x32_bf16 v[56:59], v[170:173], v[198:201], v[56:59]
	v_mfma_f32_16x16x32_bf16 v[44:47], v[156:159], v[202:205], v[44:47]
	v_mfma_f32_16x16x32_bf16 v[40:43], v[170:173], v[202:205], v[40:43]
	v_mfma_f32_16x16x32_bf16 v[28:31], v[156:159], v[214:217], v[28:31]
	v_mfma_f32_16x16x32_bf16 v[24:27], v[170:173], v[214:217], v[24:27]
	v_mfma_f32_16x16x32_bf16 v[12:15], v[156:159], v[226:229], v[12:15]
	v_mfma_f32_16x16x32_bf16 v[8:11], v[170:173], v[226:229], v[8:11]
	s_setprio 0
	s_setprio 1
	v_mfma_f32_16x16x32_bf16 v[52:55], v[174:177], v[190:193], 0
	v_mfma_f32_16x16x32_bf16 v[48:51], v[182:185], v[190:193], 0
	v_mfma_f32_16x16x32_bf16 v[36:39], v[174:177], v[194:197], 0
	v_mfma_f32_16x16x32_bf16 v[32:35], v[182:185], v[194:197], 0
	v_mfma_f32_16x16x32_bf16 v[20:23], v[174:177], v[206:209], 0
	v_mfma_f32_16x16x32_bf16 v[16:19], v[182:185], v[206:209], 0
	v_mfma_f32_16x16x32_bf16 v[4:7], v[174:177], v[210:213], 0
	v_mfma_f32_16x16x32_bf16 v[0:3], v[182:185], v[210:213], 0
	v_mfma_f32_16x16x32_bf16 v[52:55], v[178:181], v[198:201], v[52:55]
	v_mfma_f32_16x16x32_bf16 v[48:51], v[186:189], v[198:201], v[48:51]
	v_mfma_f32_16x16x32_bf16 v[36:39], v[178:181], v[202:205], v[36:39]
	v_mfma_f32_16x16x32_bf16 v[32:35], v[186:189], v[202:205], v[32:35]
	v_mfma_f32_16x16x32_bf16 v[20:23], v[178:181], v[214:217], v[20:23]
	v_mfma_f32_16x16x32_bf16 v[16:19], v[186:189], v[214:217], v[16:19]
	v_mfma_f32_16x16x32_bf16 v[4:7], v[178:181], v[226:229], v[4:7]
	v_mfma_f32_16x16x32_bf16 v[0:3], v[186:189], v[226:229], v[0:3]
	s_setprio 0
	s_barrier
	s_add_i32 s65, 0, 0x18000
	v_add_u32_e32 v151, s65, v142
	v_add_u32_e32 v156, s65, v146
	ds_read_b128 v[152:155], v151
	ds_read_b128 v[156:159], v156
	v_add_u32_e32 v151, s87, v142
	v_add_u32_e32 v170, s87, v146
	s_add_i32 s90, 0, 0x1c000
	ds_read_b128 v[166:169], v151
	ds_read_b128 v[170:173], v170
	v_add_u32_e32 v151, s90, v142
	v_add_u32_e32 v178, s90, v146
	ds_read_b128 v[174:177], v151
	ds_read_b128 v[178:181], v178
	v_add_u32_e32 v151, s2, v142
	v_add_u32_e32 v186, s2, v146
	ds_read_b128 v[182:185], v151
	ds_read_b128 v[186:189], v186
	s_add_u32 s36, s36, 0x80000
	s_addc_u32 s37, s37, 0
	s_mov_b32 m0, s57
	v_lshl_add_u64 v[232:233], s[36:37], 0, v[134:135]
	ds_read_b128 v[190:193], v147 offset:32768
	ds_read_b128 v[194:197], v147 offset:34816
	ds_read_b128 v[198:201], v148 offset:32768
	ds_read_b128 v[202:205], v148 offset:34816
	ds_read_b128 v[206:209], v147 offset:36864
	ds_read_b128 v[210:213], v147 offset:38912
	ds_read_b128 v[214:217], v148 offset:36864
	ds_read_b128 v[226:229], v148 offset:38912
	global_load_lds_dwordx4 v[232:233], off
	v_lshl_add_u64 v[232:233], s[36:37], 0, v[130:131]
	s_mov_b32 m0, s58
	s_nop 0
	global_load_lds_dwordx4 v[232:233], off
	s_waitcnt vmcnt(8)
	s_waitcnt lgkmcnt(0)
	s_barrier
	s_setprio 1
	s_waitcnt lgkmcnt(0)
	v_mfma_f32_16x16x32_bf16 v[124:127], v[152:155], v[190:193], v[124:127]
	v_mfma_f32_16x16x32_bf16 v[120:123], v[166:169], v[190:193], v[120:123]
	v_mfma_f32_16x16x32_bf16 v[112:115], v[152:155], v[194:197], v[112:115]
	v_mfma_f32_16x16x32_bf16 v[104:107], v[166:169], v[194:197], v[104:107]
	v_mfma_f32_16x16x32_bf16 v[92:95], v[152:155], v[206:209], v[92:95]
	v_mfma_f32_16x16x32_bf16 v[88:91], v[166:169], v[206:209], v[88:91]
	v_mfma_f32_16x16x32_bf16 v[76:79], v[152:155], v[210:213], v[76:79]
	v_mfma_f32_16x16x32_bf16 v[72:75], v[166:169], v[210:213], v[72:75]
	v_mfma_f32_16x16x32_bf16 v[124:127], v[156:159], v[198:201], v[124:127]
	v_mfma_f32_16x16x32_bf16 v[120:123], v[170:173], v[198:201], v[120:123]
	v_mfma_f32_16x16x32_bf16 v[112:115], v[156:159], v[202:205], v[112:115]
	v_mfma_f32_16x16x32_bf16 v[104:107], v[170:173], v[202:205], v[104:107]
	v_mfma_f32_16x16x32_bf16 v[92:95], v[156:159], v[214:217], v[92:95]
	v_mfma_f32_16x16x32_bf16 v[88:91], v[170:173], v[214:217], v[88:91]
	v_mfma_f32_16x16x32_bf16 v[76:79], v[156:159], v[226:229], v[76:79]
	v_mfma_f32_16x16x32_bf16 v[72:75], v[170:173], v[226:229], v[72:75]
	s_setprio 0
	s_setprio 1
	v_mfma_f32_16x16x32_bf16 v[116:119], v[174:177], v[190:193], v[116:119]
	v_mfma_f32_16x16x32_bf16 v[108:111], v[182:185], v[190:193], v[108:111]
	v_mfma_f32_16x16x32_bf16 v[100:103], v[174:177], v[194:197], v[100:103]
	v_mfma_f32_16x16x32_bf16 v[96:99], v[182:185], v[194:197], v[96:99]
	v_mfma_f32_16x16x32_bf16 v[84:87], v[174:177], v[206:209], v[84:87]
	v_mfma_f32_16x16x32_bf16 v[80:83], v[182:185], v[206:209], v[80:83]
	v_mfma_f32_16x16x32_bf16 v[68:71], v[174:177], v[210:213], v[68:71]
	v_mfma_f32_16x16x32_bf16 v[64:67], v[182:185], v[210:213], v[64:67]
	v_mfma_f32_16x16x32_bf16 v[116:119], v[178:181], v[198:201], v[116:119]
	v_mfma_f32_16x16x32_bf16 v[108:111], v[186:189], v[198:201], v[108:111]
	v_mfma_f32_16x16x32_bf16 v[100:103], v[178:181], v[202:205], v[100:103]
	v_mfma_f32_16x16x32_bf16 v[96:99], v[186:189], v[202:205], v[96:99]
	v_mfma_f32_16x16x32_bf16 v[84:87], v[178:181], v[214:217], v[84:87]
	v_mfma_f32_16x16x32_bf16 v[80:83], v[186:189], v[214:217], v[80:83]
	v_mfma_f32_16x16x32_bf16 v[68:71], v[178:181], v[226:229], v[68:71]
	v_mfma_f32_16x16x32_bf16 v[64:67], v[186:189], v[226:229], v[64:67]
	s_setprio 0
	s_barrier
	s_add_i32 s36, s65, s46
	v_lshl_add_u64 v[140:141], v[140:141], 0, s[54:55]
	s_mov_b32 m0, s36
	ds_read_b128 v[190:193], v147 offset:49152
	ds_read_b128 v[194:197], v147 offset:51200
	ds_read_b128 v[198:201], v148 offset:49152
	ds_read_b128 v[202:205], v148 offset:51200
	ds_read_b128 v[206:209], v147 offset:53248
	ds_read_b128 v[210:213], v147 offset:55296
	ds_read_b128 v[214:217], v148 offset:53248
	ds_read_b128 v[226:229], v148 offset:55296
	global_load_lds_dwordx4 v[140:141], off
	s_add_i32 m0, s36, 0x2000
	s_add_u32 s34, s34, 0x20080
	v_lshl_add_u64 v[140:141], v[162:163], 0, s[54:55]
	s_addc_u32 s35, s35, 0
	s_add_i32 s36, s90, s46
	global_load_lds_dwordx4 v[140:141], off
	v_lshl_add_u64 v[140:141], s[34:35], 0, v[132:133]
	s_mov_b32 m0, s36
	s_nop 0
	global_load_lds_dwordx4 v[140:141], off
	v_lshl_add_u64 v[140:141], s[34:35], 0, v[128:129]
	s_add_i32 m0, s36, 0x2000
	s_nop 0
	global_load_lds_dwordx4 v[140:141], off
	v_lshl_add_u64 v[140:141], v[218:219], 0, s[54:55]
	s_mov_b32 m0, s59
	s_nop 0
	global_load_lds_dwordx4 v[140:141], off
	v_lshl_add_u64 v[140:141], v[230:231], 0, s[54:55]
	s_mov_b32 m0, s70
	s_nop 0
	global_load_lds_dwordx4 v[140:141], off
	s_waitcnt vmcnt(8)
	s_waitcnt lgkmcnt(0)
	s_barrier
	s_setprio 1
	s_waitcnt lgkmcnt(0)
	v_mfma_f32_16x16x32_bf16 v[60:63], v[152:155], v[190:193], v[60:63]
	v_mfma_f32_16x16x32_bf16 v[56:59], v[166:169], v[190:193], v[56:59]
	v_mfma_f32_16x16x32_bf16 v[44:47], v[152:155], v[194:197], v[44:47]
	v_mfma_f32_16x16x32_bf16 v[40:43], v[166:169], v[194:197], v[40:43]
	v_mfma_f32_16x16x32_bf16 v[28:31], v[152:155], v[206:209], v[28:31]
	v_mfma_f32_16x16x32_bf16 v[24:27], v[166:169], v[206:209], v[24:27]
	v_mfma_f32_16x16x32_bf16 v[12:15], v[152:155], v[210:213], v[12:15]
	v_mfma_f32_16x16x32_bf16 v[8:11], v[166:169], v[210:213], v[8:11]
	v_mfma_f32_16x16x32_bf16 v[60:63], v[156:159], v[198:201], v[60:63]
	v_mfma_f32_16x16x32_bf16 v[56:59], v[170:173], v[198:201], v[56:59]
	v_mfma_f32_16x16x32_bf16 v[44:47], v[156:159], v[202:205], v[44:47]
	v_mfma_f32_16x16x32_bf16 v[40:43], v[170:173], v[202:205], v[40:43]
	v_mfma_f32_16x16x32_bf16 v[28:31], v[156:159], v[214:217], v[28:31]
	v_mfma_f32_16x16x32_bf16 v[24:27], v[170:173], v[214:217], v[24:27]
	v_mfma_f32_16x16x32_bf16 v[12:15], v[156:159], v[226:229], v[12:15]
	v_mfma_f32_16x16x32_bf16 v[8:11], v[170:173], v[226:229], v[8:11]
	s_setprio 0
	s_setprio 1
	v_mfma_f32_16x16x32_bf16 v[52:55], v[174:177], v[190:193], v[52:55]
	v_mfma_f32_16x16x32_bf16 v[48:51], v[182:185], v[190:193], v[48:51]
	v_mfma_f32_16x16x32_bf16 v[36:39], v[174:177], v[194:197], v[36:39]
	v_mfma_f32_16x16x32_bf16 v[32:35], v[182:185], v[194:197], v[32:35]
	v_mfma_f32_16x16x32_bf16 v[20:23], v[174:177], v[206:209], v[20:23]
	v_mfma_f32_16x16x32_bf16 v[16:19], v[182:185], v[206:209], v[16:19]
	v_mfma_f32_16x16x32_bf16 v[4:7], v[174:177], v[210:213], v[4:7]
	v_mfma_f32_16x16x32_bf16 v[0:3], v[182:185], v[210:213], v[0:3]
	v_mfma_f32_16x16x32_bf16 v[52:55], v[178:181], v[198:201], v[52:55]
	v_mfma_f32_16x16x32_bf16 v[48:51], v[186:189], v[198:201], v[48:51]
	v_mfma_f32_16x16x32_bf16 v[36:39], v[178:181], v[202:205], v[36:39]
	v_mfma_f32_16x16x32_bf16 v[32:35], v[186:189], v[202:205], v[32:35]
	v_mfma_f32_16x16x32_bf16 v[20:23], v[178:181], v[214:217], v[20:23]
	v_mfma_f32_16x16x32_bf16 v[16:19], v[186:189], v[214:217], v[16:19]
	v_mfma_f32_16x16x32_bf16 v[4:7], v[178:181], v[226:229], v[4:7]
	v_mfma_f32_16x16x32_bf16 v[0:3], v[186:189], v[226:229], v[0:3]
	s_setprio 0
	s_barrier
	s_add_i32 s89, s89, 2
	s_add_u32 s30, s30, 0x100
	s_addc_u32 s31, s31, 0
	s_add_u32 s84, s84, 0x100
	s_addc_u32 s88, s88, 0
	s_cmp_gt_u32 s89, 29
	s_cbranch_scc1 .Lepi_1040

.LBB0_1090:
	s_ashr_i32 s17, s16, 31
	s_lshl_b64 s[18:19], s[16:17], 22
	s_add_u32 s18, s50, s18
	s_addc_u32 s19, s51, s19
	s_and_b64 s[20:21], s[6:7], exec
	s_cselect_b32 s17, s19, s31
	s_cselect_b32 s73, s18, s30
	s_ashr_i32 s11, s10, 31
	s_lshl_b64 s[20:21], s[10:11], 22
	s_add_u32 s20, s41, s20
	s_addc_u32 s21, s43, s21
	s_and_b64 s[36:37], s[6:7], exec
	s_cselect_b32 s11, s21, s35
	s_cselect_b32 s76, s20, s34
	s_add_u32 s30, s30, 0x200080
	s_addc_u32 s31, s31, 0
	s_add_u32 s77, s34, 0x100
	s_addc_u32 s84, s35, 0
	s_mov_b32 s88, -2
	s_add_u32 s34, s30, 0xffe00080
	s_addc_u32 s35, s31, -1
	s_add_i32 s65, 0, 0x10000
	s_cmpk_eq_i32 s88, 0x7c
	v_add_u32_e32 v149, s65, v140
	v_add_u32_e32 v154, s65, v144
	s_cselect_b32 s37, s17, s35
	s_cselect_b32 s36, s73, s34
	ds_read_b128 v[150:153], v149
	ds_read_b128 v[154:157], v154
	v_add_u32_e32 v149, s1, v140
	s_cselect_b32 s35, s11, s84
	s_cselect_b32 s34, s76, s77
	s_add_i32 s89, 0, 0x14000
	v_add_u32_e32 v158, s1, v144
	ds_read_b128 v[166:169], v149
	ds_read_b128 v[170:173], v158
	v_add_u32_e32 v149, s89, v140
	v_add_u32_e32 v158, s89, v144
	ds_read_b128 v[174:177], v149
	ds_read_b128 v[178:181], v158
	v_add_u32_e32 v149, s86, v140
	v_add_u32_e32 v158, s86, v144
	ds_read_b128 v[182:185], v149
	ds_read_b128 v[186:189], v158
	v_lshl_add_u64 v[158:159], s[30:31], 0, v[136:137]
	s_add_i32 m0, s47, 0xc000
	ds_read_b128 v[190:193], v145
	ds_read_b128 v[194:197], v145 offset:2048
	ds_read_b128 v[198:201], v146
	ds_read_b128 v[202:205], v146 offset:2048
	ds_read_b128 v[206:209], v145 offset:4096
	ds_read_b128 v[210:213], v145 offset:6144
	ds_read_b128 v[214:217], v146 offset:4096
	ds_read_b128 v[226:229], v146 offset:6144
	global_load_lds_dwordx4 v[158:159], off
	v_lshl_add_u64 v[158:159], s[30:31], 0, v[138:139]
	s_add_i32 m0, s47, 0xe000
	s_nop 0
	global_load_lds_dwordx4 v[158:159], off
	s_waitcnt vmcnt(8)
	s_waitcnt lgkmcnt(0)
	s_barrier
	s_setprio 1
	s_waitcnt lgkmcnt(0)
	v_mfma_f32_16x16x32_bf16 v[124:127], v[150:153], v[190:193], 0
	v_mfma_f32_16x16x32_bf16 v[120:123], v[166:169], v[190:193], 0
	v_mfma_f32_16x16x32_bf16 v[116:119], v[150:153], v[194:197], 0
	v_mfma_f32_16x16x32_bf16 v[112:115], v[166:169], v[194:197], 0
	v_mfma_f32_16x16x32_bf16 v[100:103], v[150:153], v[206:209], 0
	v_mfma_f32_16x16x32_bf16 v[96:99], v[166:169], v[206:209], 0
	v_mfma_f32_16x16x32_bf16 v[84:87], v[150:153], v[210:213], 0
	v_mfma_f32_16x16x32_bf16 v[76:79], v[166:169], v[210:213], 0
	v_mfma_f32_16x16x32_bf16 v[124:127], v[154:157], v[198:201], v[124:127]
	v_mfma_f32_16x16x32_bf16 v[120:123], v[170:173], v[198:201], v[120:123]
	v_mfma_f32_16x16x32_bf16 v[116:119], v[154:157], v[202:205], v[116:119]
	v_mfma_f32_16x16x32_bf16 v[112:115], v[170:173], v[202:205], v[112:115]
	v_mfma_f32_16x16x32_bf16 v[100:103], v[154:157], v[214:217], v[100:103]
	v_mfma_f32_16x16x32_bf16 v[96:99], v[170:173], v[214:217], v[96:99]
	v_mfma_f32_16x16x32_bf16 v[84:87], v[154:157], v[226:229], v[84:87]
	v_mfma_f32_16x16x32_bf16 v[76:79], v[170:173], v[226:229], v[76:79]
	s_setprio 0
	s_setprio 1
	v_mfma_f32_16x16x32_bf16 v[108:111], v[174:177], v[190:193], 0
	v_mfma_f32_16x16x32_bf16 v[104:107], v[182:185], v[190:193], 0
	v_mfma_f32_16x16x32_bf16 v[92:95], v[174:177], v[194:197], 0
	v_mfma_f32_16x16x32_bf16 v[88:91], v[182:185], v[194:197], 0
	v_mfma_f32_16x16x32_bf16 v[80:83], v[174:177], v[206:209], 0
	v_mfma_f32_16x16x32_bf16 v[72:75], v[182:185], v[206:209], 0
	v_mfma_f32_16x16x32_bf16 v[68:71], v[174:177], v[210:213], 0
	v_mfma_f32_16x16x32_bf16 v[64:67], v[182:185], v[210:213], 0
	v_mfma_f32_16x16x32_bf16 v[108:111], v[178:181], v[198:201], v[108:111]
	v_mfma_f32_16x16x32_bf16 v[104:107], v[186:189], v[198:201], v[104:107]
	v_mfma_f32_16x16x32_bf16 v[92:95], v[178:181], v[202:205], v[92:95]
	v_mfma_f32_16x16x32_bf16 v[88:91], v[186:189], v[202:205], v[88:91]
	v_mfma_f32_16x16x32_bf16 v[80:83], v[178:181], v[214:217], v[80:83]
	v_mfma_f32_16x16x32_bf16 v[72:75], v[186:189], v[214:217], v[72:75]
	v_mfma_f32_16x16x32_bf16 v[68:71], v[178:181], v[226:229], v[68:71]
	v_mfma_f32_16x16x32_bf16 v[64:67], v[186:189], v[226:229], v[64:67]
	s_setprio 0
	s_barrier
	s_add_i32 s65, s65, s46
	v_lshl_add_u64 v[158:159], s[34:35], 0, v[132:133]
	s_mov_b32 m0, s65
	ds_read_b128 v[190:193], v145 offset:16384
	ds_read_b128 v[194:197], v145 offset:18432
	ds_read_b128 v[198:201], v146 offset:16384
	ds_read_b128 v[202:205], v146 offset:18432
	ds_read_b128 v[206:209], v145 offset:20480
	ds_read_b128 v[210:213], v145 offset:22528
	ds_read_b128 v[214:217], v146 offset:20480
	ds_read_b128 v[226:229], v146 offset:22528
	global_load_lds_dwordx4 v[158:159], off
	s_add_i32 m0, s65, 0x2000
	s_add_u32 s90, s34, 0x80000
	v_lshl_add_u64 v[162:163], s[34:35], 0, v[128:129]
	s_addc_u32 s91, s35, 0
	s_add_i32 s65, s89, s46
	global_load_lds_dwordx4 v[162:163], off
	v_lshl_add_u64 v[218:219], s[90:91], 0, v[132:133]
	s_mov_b32 m0, s65
	v_lshl_add_u64 v[230:231], s[36:37], 0, v[130:131]
	global_load_lds_dwordx4 v[218:219], off
	v_lshl_add_u64 v[218:219], s[90:91], 0, v[128:129]
	s_add_i32 m0, s65, 0x2000
	s_nop 0
	global_load_lds_dwordx4 v[218:219], off
	v_lshl_add_u64 v[218:219], s[36:37], 0, v[134:135]
	s_mov_b32 m0, s47
	s_nop 0
	global_load_lds_dwordx4 v[218:219], off
	s_mov_b32 m0, s56
	s_nop 0
	global_load_lds_dwordx4 v[230:231], off
	s_waitcnt vmcnt(8)
	s_waitcnt lgkmcnt(0)
	s_barrier
	s_setprio 1
	s_waitcnt lgkmcnt(0)
	v_mfma_f32_16x16x32_bf16 v[60:63], v[150:153], v[190:193], 0
	v_mfma_f32_16x16x32_bf16 v[56:59], v[166:169], v[190:193], 0
	v_mfma_f32_16x16x32_bf16 v[52:55], v[150:153], v[194:197], 0
	v_mfma_f32_16x16x32_bf16 v[44:47], v[166:169], v[194:197], 0
	v_mfma_f32_16x16x32_bf16 v[36:39], v[150:153], v[206:209], 0
	v_mfma_f32_16x16x32_bf16 v[28:31], v[166:169], v[206:209], 0
	v_mfma_f32_16x16x32_bf16 v[20:23], v[150:153], v[210:213], 0
	v_mfma_f32_16x16x32_bf16 v[12:15], v[166:169], v[210:213], 0
	v_mfma_f32_16x16x32_bf16 v[60:63], v[154:157], v[198:201], v[60:63]
	v_mfma_f32_16x16x32_bf16 v[56:59], v[170:173], v[198:201], v[56:59]
	v_mfma_f32_16x16x32_bf16 v[52:55], v[154:157], v[202:205], v[52:55]
	v_mfma_f32_16x16x32_bf16 v[44:47], v[170:173], v[202:205], v[44:47]
	v_mfma_f32_16x16x32_bf16 v[36:39], v[154:157], v[214:217], v[36:39]
	v_mfma_f32_16x16x32_bf16 v[28:31], v[170:173], v[214:217], v[28:31]
	v_mfma_f32_16x16x32_bf16 v[20:23], v[154:157], v[226:229], v[20:23]
	v_mfma_f32_16x16x32_bf16 v[12:15], v[170:173], v[226:229], v[12:15]
	s_setprio 0
	s_setprio 1
	v_mfma_f32_16x16x32_bf16 v[48:51], v[174:177], v[190:193], 0
	v_mfma_f32_16x16x32_bf16 v[40:43], v[182:185], v[190:193], 0
	v_mfma_f32_16x16x32_bf16 v[32:35], v[174:177], v[194:197], 0
	v_mfma_f32_16x16x32_bf16 v[24:27], v[182:185], v[194:197], 0
	v_mfma_f32_16x16x32_bf16 v[16:19], v[174:177], v[206:209], 0
	v_mfma_f32_16x16x32_bf16 v[8:11], v[182:185], v[206:209], 0
	v_mfma_f32_16x16x32_bf16 v[4:7], v[174:177], v[210:213], 0
	v_mfma_f32_16x16x32_bf16 v[0:3], v[182:185], v[210:213], 0
	v_mfma_f32_16x16x32_bf16 v[48:51], v[178:181], v[198:201], v[48:51]
	v_mfma_f32_16x16x32_bf16 v[40:43], v[186:189], v[198:201], v[40:43]
	v_mfma_f32_16x16x32_bf16 v[32:35], v[178:181], v[202:205], v[32:35]
	v_mfma_f32_16x16x32_bf16 v[24:27], v[186:189], v[202:205], v[24:27]
	v_mfma_f32_16x16x32_bf16 v[16:19], v[178:181], v[214:217], v[16:19]
	v_mfma_f32_16x16x32_bf16 v[8:11], v[186:189], v[214:217], v[8:11]
	v_mfma_f32_16x16x32_bf16 v[4:7], v[178:181], v[226:229], v[4:7]
	v_mfma_f32_16x16x32_bf16 v[0:3], v[186:189], v[226:229], v[0:3]
	s_setprio 0
	s_barrier
	s_add_i32 s65, 0, 0x18000
	v_add_u32_e32 v149, s65, v140
	v_add_u32_e32 v154, s65, v144
	ds_read_b128 v[150:153], v149
	ds_read_b128 v[154:157], v154
	v_add_u32_e32 v149, s87, v140
	v_add_u32_e32 v170, s87, v144
	s_add_i32 s89, 0, 0x1c000
	ds_read_b128 v[166:169], v149
	ds_read_b128 v[170:173], v170
	v_add_u32_e32 v149, s89, v140
	v_add_u32_e32 v178, s89, v144
	ds_read_b128 v[174:177], v149
	ds_read_b128 v[178:181], v178
	v_add_u32_e32 v149, s2, v140
	v_add_u32_e32 v186, s2, v144
	ds_read_b128 v[182:185], v149
	ds_read_b128 v[186:189], v186
	s_add_u32 s36, s36, 0x200000
	s_addc_u32 s37, s37, 0
	s_mov_b32 m0, s57
	v_lshl_add_u64 v[232:233], s[36:37], 0, v[134:135]
	ds_read_b128 v[190:193], v145 offset:32768
	ds_read_b128 v[194:197], v145 offset:34816
	ds_read_b128 v[198:201], v146 offset:32768
	ds_read_b128 v[202:205], v146 offset:34816
	ds_read_b128 v[206:209], v145 offset:36864
	ds_read_b128 v[210:213], v145 offset:38912
	ds_read_b128 v[214:217], v146 offset:36864
	ds_read_b128 v[226:229], v146 offset:38912
	global_load_lds_dwordx4 v[232:233], off
	v_lshl_add_u64 v[232:233], s[36:37], 0, v[130:131]
	s_mov_b32 m0, s58
	s_nop 0
	global_load_lds_dwordx4 v[232:233], off
	s_waitcnt vmcnt(8)
	s_waitcnt lgkmcnt(0)
	s_barrier
	s_setprio 1
	s_waitcnt lgkmcnt(0)
	v_mfma_f32_16x16x32_bf16 v[124:127], v[150:153], v[190:193], v[124:127]
	v_mfma_f32_16x16x32_bf16 v[120:123], v[166:169], v[190:193], v[120:123]
	v_mfma_f32_16x16x32_bf16 v[116:119], v[150:153], v[194:197], v[116:119]
	v_mfma_f32_16x16x32_bf16 v[112:115], v[166:169], v[194:197], v[112:115]
	v_mfma_f32_16x16x32_bf16 v[100:103], v[150:153], v[206:209], v[100:103]
	v_mfma_f32_16x16x32_bf16 v[96:99], v[166:169], v[206:209], v[96:99]
	v_mfma_f32_16x16x32_bf16 v[84:87], v[150:153], v[210:213], v[84:87]
	v_mfma_f32_16x16x32_bf16 v[76:79], v[166:169], v[210:213], v[76:79]
	v_mfma_f32_16x16x32_bf16 v[124:127], v[154:157], v[198:201], v[124:127]
	v_mfma_f32_16x16x32_bf16 v[120:123], v[170:173], v[198:201], v[120:123]
	v_mfma_f32_16x16x32_bf16 v[116:119], v[154:157], v[202:205], v[116:119]
	v_mfma_f32_16x16x32_bf16 v[112:115], v[170:173], v[202:205], v[112:115]
	v_mfma_f32_16x16x32_bf16 v[100:103], v[154:157], v[214:217], v[100:103]
	v_mfma_f32_16x16x32_bf16 v[96:99], v[170:173], v[214:217], v[96:99]
	v_mfma_f32_16x16x32_bf16 v[84:87], v[154:157], v[226:229], v[84:87]
	v_mfma_f32_16x16x32_bf16 v[76:79], v[170:173], v[226:229], v[76:79]
	s_setprio 0
	s_setprio 1
	v_mfma_f32_16x16x32_bf16 v[108:111], v[174:177], v[190:193], v[108:111]
	v_mfma_f32_16x16x32_bf16 v[104:107], v[182:185], v[190:193], v[104:107]
	v_mfma_f32_16x16x32_bf16 v[92:95], v[174:177], v[194:197], v[92:95]
	v_mfma_f32_16x16x32_bf16 v[88:91], v[182:185], v[194:197], v[88:91]
	v_mfma_f32_16x16x32_bf16 v[80:83], v[174:177], v[206:209], v[80:83]
	v_mfma_f32_16x16x32_bf16 v[72:75], v[182:185], v[206:209], v[72:75]
	v_mfma_f32_16x16x32_bf16 v[68:71], v[174:177], v[210:213], v[68:71]
	v_mfma_f32_16x16x32_bf16 v[64:67], v[182:185], v[210:213], v[64:67]
	v_mfma_f32_16x16x32_bf16 v[108:111], v[178:181], v[198:201], v[108:111]
	v_mfma_f32_16x16x32_bf16 v[104:107], v[186:189], v[198:201], v[104:107]
	v_mfma_f32_16x16x32_bf16 v[92:95], v[178:181], v[202:205], v[92:95]
	v_mfma_f32_16x16x32_bf16 v[88:91], v[186:189], v[202:205], v[88:91]
	v_mfma_f32_16x16x32_bf16 v[80:83], v[178:181], v[214:217], v[80:83]
	v_mfma_f32_16x16x32_bf16 v[72:75], v[186:189], v[214:217], v[72:75]
	v_mfma_f32_16x16x32_bf16 v[68:71], v[178:181], v[226:229], v[68:71]
	v_mfma_f32_16x16x32_bf16 v[64:67], v[186:189], v[226:229], v[64:67]
	s_setprio 0
	s_barrier
	s_add_i32 s36, s65, s46
	v_lshl_add_u64 v[158:159], v[158:159], 0, s[54:55]
	s_mov_b32 m0, s36
	ds_read_b128 v[190:193], v145 offset:49152
	ds_read_b128 v[194:197], v145 offset:51200
	ds_read_b128 v[198:201], v146 offset:49152
	ds_read_b128 v[202:205], v146 offset:51200
	ds_read_b128 v[206:209], v145 offset:53248
	ds_read_b128 v[210:213], v145 offset:55296
	ds_read_b128 v[214:217], v146 offset:53248
	ds_read_b128 v[226:229], v146 offset:55296
	global_load_lds_dwordx4 v[158:159], off
	s_add_i32 m0, s36, 0x2000
	s_add_u32 s34, s34, 0x80080
	v_lshl_add_u64 v[158:159], v[162:163], 0, s[54:55]
	s_addc_u32 s35, s35, 0
	s_add_i32 s36, s89, s46
	global_load_lds_dwordx4 v[158:159], off
	v_lshl_add_u64 v[158:159], s[34:35], 0, v[132:133]
	s_mov_b32 m0, s36
	s_nop 0
	global_load_lds_dwordx4 v[158:159], off
	v_lshl_add_u64 v[158:159], s[34:35], 0, v[128:129]
	s_add_i32 m0, s36, 0x2000
	s_nop 0
	global_load_lds_dwordx4 v[158:159], off
	v_lshl_add_u64 v[158:159], v[218:219], 0, s[54:55]
	s_mov_b32 m0, s59
	s_nop 0
	global_load_lds_dwordx4 v[158:159], off
	v_lshl_add_u64 v[158:159], v[230:231], 0, s[54:55]
	s_mov_b32 m0, s69
	s_nop 0
	global_load_lds_dwordx4 v[158:159], off
	s_waitcnt vmcnt(8)
	s_waitcnt lgkmcnt(0)
	s_barrier
	s_setprio 1
	s_waitcnt lgkmcnt(0)
	v_mfma_f32_16x16x32_bf16 v[60:63], v[150:153], v[190:193], v[60:63]
	v_mfma_f32_16x16x32_bf16 v[56:59], v[166:169], v[190:193], v[56:59]
	v_mfma_f32_16x16x32_bf16 v[52:55], v[150:153], v[194:197], v[52:55]
	v_mfma_f32_16x16x32_bf16 v[44:47], v[166:169], v[194:197], v[44:47]
	v_mfma_f32_16x16x32_bf16 v[36:39], v[150:153], v[206:209], v[36:39]
	v_mfma_f32_16x16x32_bf16 v[28:31], v[166:169], v[206:209], v[28:31]
	v_mfma_f32_16x16x32_bf16 v[20:23], v[150:153], v[210:213], v[20:23]
	v_mfma_f32_16x16x32_bf16 v[12:15], v[166:169], v[210:213], v[12:15]
	v_mfma_f32_16x16x32_bf16 v[60:63], v[154:157], v[198:201], v[60:63]
	v_mfma_f32_16x16x32_bf16 v[56:59], v[170:173], v[198:201], v[56:59]
	v_mfma_f32_16x16x32_bf16 v[52:55], v[154:157], v[202:205], v[52:55]
	v_mfma_f32_16x16x32_bf16 v[44:47], v[170:173], v[202:205], v[44:47]
	v_mfma_f32_16x16x32_bf16 v[36:39], v[154:157], v[214:217], v[36:39]
	v_mfma_f32_16x16x32_bf16 v[28:31], v[170:173], v[214:217], v[28:31]
	v_mfma_f32_16x16x32_bf16 v[20:23], v[154:157], v[226:229], v[20:23]
	v_mfma_f32_16x16x32_bf16 v[12:15], v[170:173], v[226:229], v[12:15]
	s_setprio 0
	s_setprio 1
	v_mfma_f32_16x16x32_bf16 v[48:51], v[174:177], v[190:193], v[48:51]
	v_mfma_f32_16x16x32_bf16 v[40:43], v[182:185], v[190:193], v[40:43]
	v_mfma_f32_16x16x32_bf16 v[32:35], v[174:177], v[194:197], v[32:35]
	v_mfma_f32_16x16x32_bf16 v[24:27], v[182:185], v[194:197], v[24:27]
	v_mfma_f32_16x16x32_bf16 v[16:19], v[174:177], v[206:209], v[16:19]
	v_mfma_f32_16x16x32_bf16 v[8:11], v[182:185], v[206:209], v[8:11]
	v_mfma_f32_16x16x32_bf16 v[4:7], v[174:177], v[210:213], v[4:7]
	v_mfma_f32_16x16x32_bf16 v[0:3], v[182:185], v[210:213], v[0:3]
	v_mfma_f32_16x16x32_bf16 v[48:51], v[178:181], v[198:201], v[48:51]
	v_mfma_f32_16x16x32_bf16 v[40:43], v[186:189], v[198:201], v[40:43]
	v_mfma_f32_16x16x32_bf16 v[32:35], v[178:181], v[202:205], v[32:35]
	v_mfma_f32_16x16x32_bf16 v[24:27], v[186:189], v[202:205], v[24:27]
	v_mfma_f32_16x16x32_bf16 v[16:19], v[178:181], v[214:217], v[16:19]
	v_mfma_f32_16x16x32_bf16 v[8:11], v[186:189], v[214:217], v[8:11]
	v_mfma_f32_16x16x32_bf16 v[4:7], v[178:181], v[226:229], v[4:7]
	v_mfma_f32_16x16x32_bf16 v[0:3], v[186:189], v[226:229], v[0:3]
	s_setprio 0
	s_barrier
	s_add_i32 s88, s88, 2
	s_add_u32 s30, s30, 0x100
	s_addc_u32 s31, s31, 0
	s_add_u32 s77, s77, 0x100
	s_addc_u32 s84, s84, 0
	s_cmpk_gt_u32 s88, 0x7d
	s_cbranch_scc1 .Lepi_1091
